# indexer trip loop re-generated with dependency gap 12 and 7 fillers per MFMA (was 10 / 5); plus header barrier below the Q/K load issue, collect guard flags copied from vcc, q loads before the index-l
# speedup vs baseline: 1.0057x; 1.0057x over previous
.LBB0_706:
	s_or_b64 exec, exec, s[0:1]
	s_lshl_b32 s2, s16, 2
	s_andn2_b32 s2, s2, 31
	s_and_b32 s0, s16, 7
	s_and_b32 s1, s13, 1
	s_xor_b32 s6, s2, 0x3e0
	s_cmp_eq_u32 s1, 0
	s_cselect_b32 s1, s2, s6
	s_sub_i32 s6, 0x1fe0, s1
	s_lshl_b32 s25, s0, 13
	s_add_i32 s8, s6, s25
	s_lshl_b32 s2, s0, 20
	s_ashr_i32 s9, s8, 31
	s_ashr_i32 s7, s6, 5
	v_readlane_b32 s0, v254, 49
	s_add_u32 s0, s0, s2
	v_readlane_b32 s1, v254, 50
	s_addc_u32 s1, s1, 0
	s_lshl_b64 s[10:11], s[8:9], 5
	v_lshl_add_u64 v[2:3], v[146:147], 0, s[10:11]
	global_load_dwordx4 v[66:69], v[2:3], off
	global_load_dwordx4 v[70:73], v[2:3], off offset:16
	s_lshl_b64 s[8:9], s[8:9], 10
	v_lshl_add_u64 v[62:63], v[144:145], 0, s[8:9]
	global_load_dwordx4 v[2:5], v[62:63], off
	global_load_dwordx4 v[6:9], v[62:63], off offset:128
	global_load_dwordx4 v[10:13], v[62:63], off offset:256
	global_load_dwordx4 v[14:17], v[62:63], off offset:384
	global_load_dwordx4 v[18:21], v[62:63], off offset:512
	global_load_dwordx4 v[22:25], v[62:63], off offset:640
	global_load_dwordx4 v[26:29], v[62:63], off offset:768
	global_load_dwordx4 v[30:33], v[62:63], off offset:896
	global_load_dwordx4 v[34:37], v[62:63], off offset:64
	global_load_dwordx4 v[38:41], v[62:63], off offset:192
	global_load_dwordx4 v[42:45], v[62:63], off offset:320
	global_load_dwordx4 v[46:49], v[62:63], off offset:448
	global_load_dwordx4 v[50:53], v[62:63], off offset:576
	global_load_dwordx4 v[54:57], v[62:63], off offset:704
	global_load_dwordx4 v[58:61], v[62:63], off offset:832
	s_nop 0
	global_load_dwordx4 v[62:65], v[62:63], off offset:960
	v_lshl_add_u64 v[184:185], s[0:1], 0, v[152:153]
	v_lshl_add_u64 v[184:185], v[184:185], 0, v[154:155]
	s_mov_b64 s[10:11], 0x800
	v_lshl_add_u64 v[186:187], v[184:185], 0, s[10:11]
	global_load_dwordx4 v[134:137], v[184:185], off
	global_load_dwordx4 v[130:133], v[184:185], off offset:1024
	s_mov_b64 s[10:11], 0x1000
	v_lshl_add_u64 v[188:189], v[184:185], 0, s[10:11]
	global_load_dwordx4 v[126:129], v[186:187], off
	global_load_dwordx4 v[122:125], v[186:187], off offset:1024
	s_mov_b64 s[10:11], 0x1800
	v_lshl_add_u64 v[184:185], v[184:185], 0, s[10:11]
	global_load_dwordx4 v[110:113], v[188:189], off
	global_load_dwordx4 v[106:109], v[188:189], off offset:1024
	global_load_dwordx4 v[94:97], v[184:185], off
	global_load_dwordx4 v[90:93], v[184:185], off offset:1024
	s_add_i32 s7, s7, 1
	s_ashr_i32 s9, s6, 4
	s_lshl_b32 s8, s7, 1
	v_lshl_add_u64 v[172:173], s[0:1], 0, v[154:155]
	s_waitcnt lgkmcnt(0)
	s_barrier
	s_waitcnt vmcnt(23)
	v_and_b32_e32 v83, 0xffff0000, v3
	v_lshlrev_b32_e32 v82, 16, v3
	s_waitcnt vmcnt(22)
	v_and_b32_e32 v85, 0xffff0000, v7
	v_mul_f32_e32 v156, 0.5, v66
	v_mul_f32_e32 v158, 0.5, v67
	v_and_b32_e32 v67, 0xffff0000, v2
	v_lshlrev_b32_e32 v66, 16, v2
	v_mul_f32_e32 v160, 0.5, v68
	v_mul_f32_e32 v162, 0.5, v69
	v_and_b32_e32 v69, 0xffff0000, v6
	v_lshlrev_b32_e32 v68, 16, v6
	v_lshlrev_b32_e32 v84, 16, v7
	v_pk_fma_f32 v[66:67], v[156:157], v[66:67], 0 op_sel_hi:[0,1,0]
	v_pk_fma_f32 v[82:83], v[156:157], v[82:83], 0 op_sel_hi:[0,1,0]
	v_mul_f32_e32 v164, 0.5, v70
	v_mul_f32_e32 v166, 0.5, v71
	s_waitcnt vmcnt(21)
	v_and_b32_e32 v71, 0xffff0000, v10
	v_lshlrev_b32_e32 v70, 16, v10
	v_and_b32_e32 v87, 0xffff0000, v11
	v_lshlrev_b32_e32 v86, 16, v11
	v_pk_fma_f32 v[66:67], v[158:159], v[68:69], v[66:67] op_sel_hi:[0,1,1]
	v_pk_fma_f32 v[68:69], v[158:159], v[84:85], v[82:83] op_sel_hi:[0,1,1]
	v_mul_f32_e32 v168, 0.5, v72
	v_mul_f32_e32 v170, 0.5, v73
	s_waitcnt vmcnt(20)
	v_and_b32_e32 v73, 0xffff0000, v14
	v_lshlrev_b32_e32 v72, 16, v14
	v_and_b32_e32 v89, 0xffff0000, v15
	v_lshlrev_b32_e32 v88, 16, v15
	v_pk_fma_f32 v[66:67], v[160:161], v[70:71], v[66:67] op_sel_hi:[0,1,1]
	v_pk_fma_f32 v[68:69], v[160:161], v[86:87], v[68:69] op_sel_hi:[0,1,1]
	s_waitcnt vmcnt(19)
	v_and_b32_e32 v75, 0xffff0000, v18
	v_lshlrev_b32_e32 v74, 16, v18
	v_and_b32_e32 v177, 0xffff0000, v19
	v_lshlrev_b32_e32 v176, 16, v19
	v_pk_fma_f32 v[66:67], v[162:163], v[72:73], v[66:67] op_sel_hi:[0,1,1]
	v_pk_fma_f32 v[68:69], v[162:163], v[88:89], v[68:69] op_sel_hi:[0,1,1]
	s_waitcnt vmcnt(18)
	v_and_b32_e32 v77, 0xffff0000, v22
	v_lshlrev_b32_e32 v76, 16, v22
	v_and_b32_e32 v179, 0xffff0000, v23
	v_lshlrev_b32_e32 v178, 16, v23
	v_pk_fma_f32 v[66:67], v[164:165], v[74:75], v[66:67] op_sel_hi:[0,1,1]
	v_pk_fma_f32 v[68:69], v[164:165], v[176:177], v[68:69] op_sel_hi:[0,1,1]
	s_waitcnt vmcnt(17)
	v_and_b32_e32 v79, 0xffff0000, v26
	v_lshlrev_b32_e32 v78, 16, v26
	v_and_b32_e32 v181, 0xffff0000, v27
	v_lshlrev_b32_e32 v180, 16, v27
	v_pk_fma_f32 v[66:67], v[166:167], v[76:77], v[66:67] op_sel_hi:[0,1,1]
	v_pk_fma_f32 v[68:69], v[166:167], v[178:179], v[68:69] op_sel_hi:[0,1,1]
	s_waitcnt vmcnt(16)
	v_and_b32_e32 v81, 0xffff0000, v30
	v_lshlrev_b32_e32 v80, 16, v30
	v_and_b32_e32 v183, 0xffff0000, v31
	v_lshlrev_b32_e32 v182, 16, v31
	v_pk_fma_f32 v[66:67], v[168:169], v[78:79], v[66:67] op_sel_hi:[0,1,1]
	v_pk_fma_f32 v[68:69], v[168:169], v[180:181], v[68:69] op_sel_hi:[0,1,1]
	v_and_b32_e32 v99, 0xffff0000, v4
	v_lshlrev_b32_e32 v98, 16, v4
	v_pk_fma_f32 v[66:67], v[170:171], v[80:81], v[66:67] op_sel_hi:[0,1,1]
	v_pk_fma_f32 v[68:69], v[170:171], v[182:183], v[68:69] op_sel_hi:[0,1,1]
	v_cvt_pk_bf16_f32 v66, v66, v67
	v_cvt_pk_bf16_f32 v67, v68, v69
	v_pk_fma_f32 v[68:69], v[156:157], v[98:99], 0 op_sel_hi:[0,1,0]
	v_and_b32_e32 v71, 0xffff0000, v8
	v_lshlrev_b32_e32 v70, 16, v8
	v_pk_fma_f32 v[68:69], v[158:159], v[70:71], v[68:69] op_sel_hi:[0,1,1]
	v_and_b32_e32 v71, 0xffff0000, v12
	v_lshlrev_b32_e32 v70, 16, v12
	v_pk_fma_f32 v[68:69], v[160:161], v[70:71], v[68:69] op_sel_hi:[0,1,1]
	v_and_b32_e32 v71, 0xffff0000, v16
	v_lshlrev_b32_e32 v70, 16, v16
	v_pk_fma_f32 v[68:69], v[162:163], v[70:71], v[68:69] op_sel_hi:[0,1,1]
	v_and_b32_e32 v71, 0xffff0000, v20
	v_lshlrev_b32_e32 v70, 16, v20
	v_pk_fma_f32 v[68:69], v[164:165], v[70:71], v[68:69] op_sel_hi:[0,1,1]
	v_and_b32_e32 v71, 0xffff0000, v24
	v_lshlrev_b32_e32 v70, 16, v24
	v_pk_fma_f32 v[68:69], v[166:167], v[70:71], v[68:69] op_sel_hi:[0,1,1]
	v_and_b32_e32 v71, 0xffff0000, v28
	v_lshlrev_b32_e32 v70, 16, v28
	v_pk_fma_f32 v[68:69], v[168:169], v[70:71], v[68:69] op_sel_hi:[0,1,1]
	v_and_b32_e32 v71, 0xffff0000, v32
	v_lshlrev_b32_e32 v70, 16, v32
	v_pk_fma_f32 v[68:69], v[170:171], v[70:71], v[68:69] op_sel_hi:[0,1,1]
	v_and_b32_e32 v71, 0xffff0000, v5
	v_lshlrev_b32_e32 v70, 16, v5
	v_pk_fma_f32 v[70:71], v[156:157], v[70:71], 0 op_sel_hi:[0,1,0]
	v_and_b32_e32 v73, 0xffff0000, v9
	v_lshlrev_b32_e32 v72, 16, v9
	v_pk_fma_f32 v[70:71], v[158:159], v[72:73], v[70:71] op_sel_hi:[0,1,1]
	v_and_b32_e32 v73, 0xffff0000, v13
	v_lshlrev_b32_e32 v72, 16, v13
	v_pk_fma_f32 v[70:71], v[160:161], v[72:73], v[70:71] op_sel_hi:[0,1,1]
	v_and_b32_e32 v73, 0xffff0000, v17
	v_lshlrev_b32_e32 v72, 16, v17
	v_pk_fma_f32 v[70:71], v[162:163], v[72:73], v[70:71] op_sel_hi:[0,1,1]
	v_and_b32_e32 v73, 0xffff0000, v21
	v_lshlrev_b32_e32 v72, 16, v21
	v_pk_fma_f32 v[70:71], v[164:165], v[72:73], v[70:71] op_sel_hi:[0,1,1]
	v_and_b32_e32 v73, 0xffff0000, v25
	v_lshlrev_b32_e32 v72, 16, v25
	v_pk_fma_f32 v[70:71], v[166:167], v[72:73], v[70:71] op_sel_hi:[0,1,1]
	v_and_b32_e32 v73, 0xffff0000, v29
	v_lshlrev_b32_e32 v72, 16, v29
	v_pk_fma_f32 v[70:71], v[168:169], v[72:73], v[70:71] op_sel_hi:[0,1,1]
	v_and_b32_e32 v73, 0xffff0000, v33
	v_lshlrev_b32_e32 v72, 16, v33
	v_pk_fma_f32 v[70:71], v[170:171], v[72:73], v[70:71] op_sel_hi:[0,1,1]
	v_cvt_pk_bf16_f32 v68, v68, v69
	v_cvt_pk_bf16_f32 v69, v70, v71
	s_waitcnt vmcnt(15)
	v_and_b32_e32 v71, 0xffff0000, v34
	v_lshlrev_b32_e32 v70, 16, v34
	v_pk_fma_f32 v[70:71], v[156:157], v[70:71], 0 op_sel_hi:[0,1,0]
	s_waitcnt vmcnt(14)
	v_and_b32_e32 v73, 0xffff0000, v38
	v_lshlrev_b32_e32 v72, 16, v38
	v_pk_fma_f32 v[70:71], v[158:159], v[72:73], v[70:71] op_sel_hi:[0,1,1]
	s_waitcnt vmcnt(13)
	v_and_b32_e32 v73, 0xffff0000, v42
	v_lshlrev_b32_e32 v72, 16, v42
	v_pk_fma_f32 v[70:71], v[160:161], v[72:73], v[70:71] op_sel_hi:[0,1,1]
	s_waitcnt vmcnt(12)
	v_and_b32_e32 v73, 0xffff0000, v46
	v_lshlrev_b32_e32 v72, 16, v46
	v_pk_fma_f32 v[70:71], v[162:163], v[72:73], v[70:71] op_sel_hi:[0,1,1]
	s_waitcnt vmcnt(11)
	v_and_b32_e32 v73, 0xffff0000, v50
	v_lshlrev_b32_e32 v72, 16, v50
	v_pk_fma_f32 v[70:71], v[164:165], v[72:73], v[70:71] op_sel_hi:[0,1,1]
	s_waitcnt vmcnt(10)
	v_and_b32_e32 v73, 0xffff0000, v54
	v_lshlrev_b32_e32 v72, 16, v54
	v_pk_fma_f32 v[70:71], v[166:167], v[72:73], v[70:71] op_sel_hi:[0,1,1]
	s_waitcnt vmcnt(9)
	v_and_b32_e32 v73, 0xffff0000, v58
	v_lshlrev_b32_e32 v72, 16, v58
	v_pk_fma_f32 v[70:71], v[168:169], v[72:73], v[70:71] op_sel_hi:[0,1,1]
	s_waitcnt vmcnt(8)
	v_and_b32_e32 v73, 0xffff0000, v62
	v_lshlrev_b32_e32 v72, 16, v62
	v_pk_fma_f32 v[70:71], v[170:171], v[72:73], v[70:71] op_sel_hi:[0,1,1]
	v_and_b32_e32 v73, 0xffff0000, v35
	v_lshlrev_b32_e32 v72, 16, v35
	v_pk_fma_f32 v[72:73], v[156:157], v[72:73], 0 op_sel_hi:[0,1,0]
	v_and_b32_e32 v75, 0xffff0000, v39
	v_lshlrev_b32_e32 v74, 16, v39
	v_pk_fma_f32 v[72:73], v[158:159], v[74:75], v[72:73] op_sel_hi:[0,1,1]
	v_and_b32_e32 v75, 0xffff0000, v43
	v_lshlrev_b32_e32 v74, 16, v43
	v_pk_fma_f32 v[72:73], v[160:161], v[74:75], v[72:73] op_sel_hi:[0,1,1]
	v_and_b32_e32 v75, 0xffff0000, v47
	v_lshlrev_b32_e32 v74, 16, v47
	v_pk_fma_f32 v[72:73], v[162:163], v[74:75], v[72:73] op_sel_hi:[0,1,1]
	v_and_b32_e32 v75, 0xffff0000, v51
	v_lshlrev_b32_e32 v74, 16, v51
	v_pk_fma_f32 v[72:73], v[164:165], v[74:75], v[72:73] op_sel_hi:[0,1,1]
	v_and_b32_e32 v75, 0xffff0000, v55
	v_lshlrev_b32_e32 v74, 16, v55
	v_pk_fma_f32 v[72:73], v[166:167], v[74:75], v[72:73] op_sel_hi:[0,1,1]
	v_and_b32_e32 v75, 0xffff0000, v59
	v_lshlrev_b32_e32 v74, 16, v59
	v_pk_fma_f32 v[72:73], v[168:169], v[74:75], v[72:73] op_sel_hi:[0,1,1]
	v_and_b32_e32 v75, 0xffff0000, v63
	v_lshlrev_b32_e32 v74, 16, v63
	v_pk_fma_f32 v[72:73], v[170:171], v[74:75], v[72:73] op_sel_hi:[0,1,1]
	v_cvt_pk_bf16_f32 v70, v70, v71
	v_cvt_pk_bf16_f32 v71, v72, v73
	v_and_b32_e32 v73, 0xffff0000, v36
	v_lshlrev_b32_e32 v72, 16, v36
	v_pk_fma_f32 v[72:73], v[156:157], v[72:73], 0 op_sel_hi:[0,1,0]
	v_and_b32_e32 v75, 0xffff0000, v40
	v_lshlrev_b32_e32 v74, 16, v40
	v_pk_fma_f32 v[72:73], v[158:159], v[74:75], v[72:73] op_sel_hi:[0,1,1]
	v_and_b32_e32 v75, 0xffff0000, v44
	v_lshlrev_b32_e32 v74, 16, v44
	v_pk_fma_f32 v[72:73], v[160:161], v[74:75], v[72:73] op_sel_hi:[0,1,1]
	v_and_b32_e32 v75, 0xffff0000, v48
	v_lshlrev_b32_e32 v74, 16, v48
	v_pk_fma_f32 v[72:73], v[162:163], v[74:75], v[72:73] op_sel_hi:[0,1,1]
	v_and_b32_e32 v75, 0xffff0000, v52
	v_lshlrev_b32_e32 v74, 16, v52
	v_pk_fma_f32 v[72:73], v[164:165], v[74:75], v[72:73] op_sel_hi:[0,1,1]
	v_and_b32_e32 v75, 0xffff0000, v56
	v_lshlrev_b32_e32 v74, 16, v56
	v_pk_fma_f32 v[72:73], v[166:167], v[74:75], v[72:73] op_sel_hi:[0,1,1]
	v_and_b32_e32 v75, 0xffff0000, v60
	v_lshlrev_b32_e32 v74, 16, v60
	v_pk_fma_f32 v[72:73], v[168:169], v[74:75], v[72:73] op_sel_hi:[0,1,1]
	v_and_b32_e32 v75, 0xffff0000, v64
	v_lshlrev_b32_e32 v74, 16, v64
	v_pk_fma_f32 v[72:73], v[170:171], v[74:75], v[72:73] op_sel_hi:[0,1,1]
	v_and_b32_e32 v75, 0xffff0000, v37
	v_lshlrev_b32_e32 v74, 16, v37
	v_pk_fma_f32 v[74:75], v[156:157], v[74:75], 0 op_sel_hi:[0,1,0]
	v_and_b32_e32 v77, 0xffff0000, v41
	v_lshlrev_b32_e32 v76, 16, v41
	v_pk_fma_f32 v[74:75], v[158:159], v[76:77], v[74:75] op_sel_hi:[0,1,1]
	v_and_b32_e32 v77, 0xffff0000, v45
	v_lshlrev_b32_e32 v76, 16, v45
	v_pk_fma_f32 v[74:75], v[160:161], v[76:77], v[74:75] op_sel_hi:[0,1,1]
	v_and_b32_e32 v77, 0xffff0000, v49
	v_lshlrev_b32_e32 v76, 16, v49
	v_pk_fma_f32 v[74:75], v[162:163], v[76:77], v[74:75] op_sel_hi:[0,1,1]
	v_and_b32_e32 v77, 0xffff0000, v53
	v_lshlrev_b32_e32 v76, 16, v53
	v_pk_fma_f32 v[74:75], v[164:165], v[76:77], v[74:75] op_sel_hi:[0,1,1]
	v_and_b32_e32 v77, 0xffff0000, v57
	v_lshlrev_b32_e32 v76, 16, v57
	v_pk_fma_f32 v[74:75], v[166:167], v[76:77], v[74:75] op_sel_hi:[0,1,1]
	v_and_b32_e32 v77, 0xffff0000, v61
	v_lshlrev_b32_e32 v76, 16, v61
	v_pk_fma_f32 v[74:75], v[168:169], v[76:77], v[74:75] op_sel_hi:[0,1,1]
	v_and_b32_e32 v77, 0xffff0000, v65
	v_lshlrev_b32_e32 v76, 16, v65
	v_pk_fma_f32 v[74:75], v[170:171], v[76:77], v[74:75] op_sel_hi:[0,1,1]
	v_cvt_pk_bf16_f32 v72, v72, v73
	v_cvt_pk_bf16_f32 v73, v74, v75
	v_readlane_b32 s10, v254, 53
	s_waitcnt vmcnt(0)
	s_add_i32 s9, s10, s9
	s_min_i32 s9, s8, s9
	s_cmp_ge_i32 s12, s9
	s_cbranch_scc1 .LBB0_709
	v_readfirstlane_b32 s0, v138
	s_nop 3
	s_cmp_lt_u32 s0, 16
	s_cbranch_scc1 .Lstagger_skip
	s_sleep 55

.LBB0_708:
	s_mov_b32 s0, 0x20000
	s_add_i32 s52, s52, 16
	s_cmp_ge_i32 s52, s9
	v_add_u32_e32 v195, v201, v142
	v_add_u32_e32 v196, v202, v203
	s_waitcnt vmcnt(8)
	v_mfma_f32_16x16x32_bf16 v[114:117], v[134:137], v[66:69], 0
	v_mfma_f32_16x16x32_bf16 v[114:117], v[130:133], v[70:73], v[114:117]
	v_mfma_f32_16x16x32_bf16 v[74:77], v[134:137], v[2:5], 0
	v_mfma_f32_16x16x32_bf16 v[74:77], v[130:133], v[34:37], v[74:77]
	v_mfma_f32_16x16x32_bf16 v[78:81], v[134:137], v[6:9], 0
	v_mfma_f32_16x16x32_bf16 v[78:81], v[130:133], v[38:41], v[78:81]
	v_mfma_f32_16x16x32_bf16 v[82:85], v[134:137], v[10:13], 0
	v_mfma_f32_16x16x32_bf16 v[82:85], v[130:133], v[42:45], v[82:85]
	v_mfma_f32_16x16x32_bf16 v[86:89], v[134:137], v[14:17], 0
	v_mfma_f32_16x16x32_bf16 v[86:89], v[130:133], v[46:49], v[86:89]
	v_mfma_f32_16x16x32_bf16 v[98:101], v[134:137], v[18:21], 0
	v_mfma_f32_16x16x32_bf16 v[98:101], v[130:133], v[50:53], v[98:101]
	v_mfma_f32_16x16x32_bf16 v[102:105], v[134:137], v[22:25], 0
	v_mfma_f32_16x16x32_bf16 v[102:105], v[130:133], v[54:57], v[102:105]
	v_mfma_f32_16x16x32_bf16 v[224:227], v[134:137], v[26:29], 0
	v_fma_f32 v114, v156, |v74|, v114
	v_fma_f32 v115, v156, |v75|, v115
	v_fma_f32 v116, v156, |v76|, v116
	v_fma_f32 v117, v156, |v77|, v117
	v_fma_f32 v114, v158, |v78|, v114
	v_fma_f32 v115, v158, |v79|, v115
	v_fma_f32 v116, v158, |v80|, v116
	v_mfma_f32_16x16x32_bf16 v[224:227], v[130:133], v[58:61], v[224:227]
	v_fma_f32 v117, v158, |v81|, v117
	v_fma_f32 v114, v160, |v82|, v114
	v_fma_f32 v115, v160, |v83|, v115
	v_fma_f32 v116, v160, |v84|, v116
	v_fma_f32 v117, v160, |v85|, v117
	v_fma_f32 v114, v162, |v86|, v114
	v_fma_f32 v115, v162, |v87|, v115
	v_mfma_f32_16x16x32_bf16 v[228:231], v[134:137], v[30:33], 0
	v_fma_f32 v116, v162, |v88|, v116
	v_fma_f32 v117, v162, |v89|, v117
	v_fma_f32 v114, v164, |v98|, v114
	v_fma_f32 v115, v164, |v99|, v115
	v_fma_f32 v116, v164, |v100|, v116
	v_fma_f32 v117, v164, |v101|, v117
	v_fma_f32 v114, v166, |v102|, v114
	v_mfma_f32_16x16x32_bf16 v[228:231], v[130:133], v[62:65], v[228:231]
	v_fma_f32 v115, v166, |v103|, v115
	v_fma_f32 v116, v166, |v104|, v116
	v_fma_f32 v117, v166, |v105|, v117
	v_fma_f32 v114, v168, |v224|, v114
	v_fma_f32 v115, v168, |v225|, v115
	v_fma_f32 v116, v168, |v226|, v116
	v_fma_f32 v117, v168, |v227|, v117
	v_add_u32_e32 v194, -48, v157
	v_min_u32_e32 v194, 0x1fff, v194
	v_lshlrev_b32_e32 v140, 7, v194
	v_lshl_add_u64 v[192:193], v[172:173], 0, v[140:141]
	global_load_dwordx4 v[134:137], v[192:193], off
	global_load_dwordx4 v[130:133], v[192:193], off offset:1024
	s_waitcnt vmcnt(8)
	v_mfma_f32_16x16x32_bf16 v[118:121], v[126:129], v[66:69], 0
	v_fma_f32 v114, v170, |v228|, v114
	v_fma_f32 v115, v170, |v229|, v115
	v_fma_f32 v116, v170, |v230|, v116
	v_fma_f32 v117, v170, |v231|, v117
	v_cvt_pk_f16_f32 v184, v114, v115
	v_cvt_pk_f16_f32 v185, v116, v117
	v_pk_ashrrev_i16 v186, 15, v184 op_sel_hi:[0,1]
	v_mfma_f32_16x16x32_bf16 v[118:121], v[122:125], v[70:73], v[118:121]
	v_bitop3_b32 v176, v186, v184, s3 bitop3:0x36
	v_pk_ashrrev_i16 v186, 15, v185 op_sel_hi:[0,1]
	v_bitop3_b32 v177, v186, v185, s3 bitop3:0x36
	v_bfe_u32 v188, v176, 7, 9
	v_lshrrev_b32_e32 v189, 23, v176
	v_bfe_u32 v190, v177, 7, 9
	v_lshrrev_b32_e32 v191, 23, v177
	v_mfma_f32_16x16x32_bf16 v[74:77], v[126:129], v[2:5], 0
	v_lshl_add_u32 v188, v188, 2, v143
	v_lshl_add_u32 v189, v189, 2, v143
	v_lshl_add_u32 v190, v190, 2, v143
	v_lshl_add_u32 v191, v191, 2, v143
	ds_add_u32 v188, v206
	ds_add_u32 v189, v206
	ds_add_u32 v190, v206
	v_mfma_f32_16x16x32_bf16 v[74:77], v[122:125], v[34:37], v[74:77]
	ds_add_u32 v191, v206
	v_mfma_f32_16x16x32_bf16 v[78:81], v[126:129], v[6:9], 0
	v_mfma_f32_16x16x32_bf16 v[78:81], v[122:125], v[38:41], v[78:81]
	v_mfma_f32_16x16x32_bf16 v[82:85], v[126:129], v[10:13], 0
	v_mfma_f32_16x16x32_bf16 v[82:85], v[122:125], v[42:45], v[82:85]
	v_mfma_f32_16x16x32_bf16 v[86:89], v[126:129], v[14:17], 0
	v_mfma_f32_16x16x32_bf16 v[86:89], v[122:125], v[46:49], v[86:89]
	v_mfma_f32_16x16x32_bf16 v[98:101], v[126:129], v[18:21], 0
	v_mfma_f32_16x16x32_bf16 v[98:101], v[122:125], v[50:53], v[98:101]
	v_mfma_f32_16x16x32_bf16 v[102:105], v[126:129], v[22:25], 0
	v_mfma_f32_16x16x32_bf16 v[102:105], v[122:125], v[54:57], v[102:105]
	v_fma_f32 v118, v156, |v74|, v118
	v_fma_f32 v119, v156, |v75|, v119
	v_fma_f32 v120, v156, |v76|, v120
	v_fma_f32 v121, v156, |v77|, v121
	v_fma_f32 v118, v158, |v78|, v118
	v_fma_f32 v119, v158, |v79|, v119
	v_fma_f32 v120, v158, |v80|, v120
	v_mfma_f32_16x16x32_bf16 v[224:227], v[126:129], v[26:29], 0
	v_fma_f32 v121, v158, |v81|, v121
	v_fma_f32 v118, v160, |v82|, v118
	v_fma_f32 v119, v160, |v83|, v119
	v_fma_f32 v120, v160, |v84|, v120
	v_fma_f32 v121, v160, |v85|, v121
	v_fma_f32 v118, v162, |v86|, v118
	v_fma_f32 v119, v162, |v87|, v119
	v_mfma_f32_16x16x32_bf16 v[224:227], v[122:125], v[58:61], v[224:227]
	v_fma_f32 v120, v162, |v88|, v120
	v_fma_f32 v121, v162, |v89|, v121
	v_fma_f32 v118, v164, |v98|, v118
	v_fma_f32 v119, v164, |v99|, v119
	v_fma_f32 v120, v164, |v100|, v120
	v_fma_f32 v121, v164, |v101|, v121
	v_fma_f32 v118, v166, |v102|, v118
	v_mfma_f32_16x16x32_bf16 v[228:231], v[126:129], v[30:33], 0
	v_fma_f32 v119, v166, |v103|, v119
	v_fma_f32 v120, v166, |v104|, v120
	v_fma_f32 v121, v166, |v105|, v121
	v_fma_f32 v118, v168, |v224|, v118
	v_fma_f32 v119, v168, |v225|, v119
	v_fma_f32 v120, v168, |v226|, v120
	v_fma_f32 v121, v168, |v227|, v121
	v_mfma_f32_16x16x32_bf16 v[228:231], v[122:125], v[62:65], v[228:231]
	v_add_u32_e32 v194, -32, v157
	v_min_u32_e32 v194, 0x1fff, v194
	v_lshlrev_b32_e32 v140, 7, v194
	v_lshl_add_u64 v[192:193], v[172:173], 0, v[140:141]
	global_load_dwordx4 v[126:129], v[192:193], off
	global_load_dwordx4 v[122:125], v[192:193], off offset:1024
	s_waitcnt vmcnt(8)
	v_mfma_f32_16x16x32_bf16 v[114:117], v[110:113], v[66:69], 0
	v_mfma_f32_16x16x32_bf16 v[114:117], v[106:109], v[70:73], v[114:117]
	v_mfma_f32_16x16x32_bf16 v[74:77], v[110:113], v[2:5], 0
	v_mfma_f32_16x16x32_bf16 v[74:77], v[106:109], v[34:37], v[74:77]
	v_fma_f32 v118, v170, |v228|, v118
	v_fma_f32 v119, v170, |v229|, v119
	v_fma_f32 v120, v170, |v230|, v120
	v_fma_f32 v121, v170, |v231|, v121
	v_cvt_pk_f16_f32 v184, v118, v119
	v_cvt_pk_f16_f32 v185, v120, v121
	v_pk_ashrrev_i16 v186, 15, v184 op_sel_hi:[0,1]
	v_mfma_f32_16x16x32_bf16 v[78:81], v[110:113], v[6:9], 0
	v_bitop3_b32 v178, v186, v184, s3 bitop3:0x36
	v_pk_ashrrev_i16 v186, 15, v185 op_sel_hi:[0,1]
	v_bitop3_b32 v179, v186, v185, s3 bitop3:0x36
	v_bfe_u32 v188, v178, 7, 9
	v_lshrrev_b32_e32 v189, 23, v178
	v_bfe_u32 v190, v179, 7, 9
	v_lshrrev_b32_e32 v191, 23, v179
	v_mfma_f32_16x16x32_bf16 v[78:81], v[106:109], v[38:41], v[78:81]
	v_lshl_add_u32 v188, v188, 2, v143
	v_lshl_add_u32 v189, v189, 2, v143
	v_lshl_add_u32 v190, v190, 2, v143
	v_lshl_add_u32 v191, v191, 2, v143
	ds_add_u32 v188, v206
	ds_add_u32 v189, v206
	ds_add_u32 v190, v206
	v_mfma_f32_16x16x32_bf16 v[82:85], v[110:113], v[10:13], 0
	ds_add_u32 v191, v206
	v_fma_f32 v114, v156, |v74|, v114
	v_fma_f32 v115, v156, |v75|, v115
	v_fma_f32 v116, v156, |v76|, v116
	v_fma_f32 v117, v156, |v77|, v117
	v_fma_f32 v114, v158, |v78|, v114
	v_fma_f32 v115, v158, |v79|, v115
	v_mfma_f32_16x16x32_bf16 v[82:85], v[106:109], v[42:45], v[82:85]
	v_fma_f32 v116, v158, |v80|, v116
	v_fma_f32 v117, v158, |v81|, v117
	v_mfma_f32_16x16x32_bf16 v[86:89], v[110:113], v[14:17], 0
	v_mfma_f32_16x16x32_bf16 v[86:89], v[106:109], v[46:49], v[86:89]
	v_mfma_f32_16x16x32_bf16 v[98:101], v[110:113], v[18:21], 0
	v_mfma_f32_16x16x32_bf16 v[98:101], v[106:109], v[50:53], v[98:101]
	v_mfma_f32_16x16x32_bf16 v[102:105], v[110:113], v[22:25], 0
	v_mfma_f32_16x16x32_bf16 v[102:105], v[106:109], v[54:57], v[102:105]
	v_mfma_f32_16x16x32_bf16 v[224:227], v[110:113], v[26:29], 0
	v_mfma_f32_16x16x32_bf16 v[224:227], v[106:109], v[58:61], v[224:227]
	v_mfma_f32_16x16x32_bf16 v[228:231], v[110:113], v[30:33], 0
	v_fma_f32 v114, v160, |v82|, v114
	v_fma_f32 v115, v160, |v83|, v115
	v_fma_f32 v116, v160, |v84|, v116
	v_fma_f32 v117, v160, |v85|, v117
	v_fma_f32 v114, v162, |v86|, v114
	v_fma_f32 v115, v162, |v87|, v115
	v_fma_f32 v116, v162, |v88|, v116
	v_mfma_f32_16x16x32_bf16 v[228:231], v[106:109], v[62:65], v[228:231]
	v_fma_f32 v117, v162, |v89|, v117
	v_fma_f32 v114, v164, |v98|, v114
	v_fma_f32 v115, v164, |v99|, v115
	v_fma_f32 v116, v164, |v100|, v116
	v_fma_f32 v117, v164, |v101|, v117
	v_fma_f32 v114, v166, |v102|, v114
	v_fma_f32 v115, v166, |v103|, v115
	v_add_u32_e32 v194, -16, v157
	v_min_u32_e32 v194, 0x1fff, v194
	v_lshlrev_b32_e32 v140, 7, v194
	v_lshl_add_u64 v[192:193], v[172:173], 0, v[140:141]
	global_load_dwordx4 v[110:113], v[192:193], off
	global_load_dwordx4 v[106:109], v[192:193], off offset:1024
	s_waitcnt vmcnt(8)
	v_mfma_f32_16x16x32_bf16 v[118:121], v[94:97], v[66:69], 0
	v_fma_f32 v116, v166, |v104|, v116
	v_fma_f32 v117, v166, |v105|, v117
	v_fma_f32 v114, v168, |v224|, v114
	v_fma_f32 v115, v168, |v225|, v115
	v_fma_f32 v116, v168, |v226|, v116
	v_fma_f32 v117, v168, |v227|, v117
	v_fma_f32 v114, v170, |v228|, v114
	v_mfma_f32_16x16x32_bf16 v[118:121], v[90:93], v[70:73], v[118:121]
	v_fma_f32 v115, v170, |v229|, v115
	v_fma_f32 v116, v170, |v230|, v116
	v_fma_f32 v117, v170, |v231|, v117
	v_cvt_pk_f16_f32 v184, v114, v115
	v_cvt_pk_f16_f32 v185, v116, v117
	v_pk_ashrrev_i16 v186, 15, v184 op_sel_hi:[0,1]
	v_bitop3_b32 v180, v186, v184, s3 bitop3:0x36
	v_mfma_f32_16x16x32_bf16 v[74:77], v[94:97], v[2:5], 0
	v_pk_ashrrev_i16 v186, 15, v185 op_sel_hi:[0,1]
	v_bitop3_b32 v181, v186, v185, s3 bitop3:0x36
	v_bfe_u32 v188, v180, 7, 9
	v_lshrrev_b32_e32 v189, 23, v180
	v_bfe_u32 v190, v181, 7, 9
	v_lshrrev_b32_e32 v191, 23, v181
	v_lshl_add_u32 v188, v188, 2, v143
	v_mfma_f32_16x16x32_bf16 v[74:77], v[90:93], v[34:37], v[74:77]
	v_lshl_add_u32 v189, v189, 2, v143
	v_lshl_add_u32 v190, v190, 2, v143
	v_lshl_add_u32 v191, v191, 2, v143
	ds_add_u32 v188, v206
	ds_add_u32 v189, v206
	ds_add_u32 v190, v206
	ds_add_u32 v191, v206
	v_mfma_f32_16x16x32_bf16 v[78:81], v[94:97], v[6:9], 0
	v_mfma_f32_16x16x32_bf16 v[78:81], v[90:93], v[38:41], v[78:81]
	v_mfma_f32_16x16x32_bf16 v[82:85], v[94:97], v[10:13], 0
	v_mfma_f32_16x16x32_bf16 v[82:85], v[90:93], v[42:45], v[82:85]
	v_fma_f32 v118, v156, |v74|, v118
	v_fma_f32 v119, v156, |v75|, v119
	v_fma_f32 v120, v156, |v76|, v120
	v_fma_f32 v121, v156, |v77|, v121
	v_mfma_f32_16x16x32_bf16 v[86:89], v[94:97], v[14:17], 0
	v_mfma_f32_16x16x32_bf16 v[86:89], v[90:93], v[46:49], v[86:89]
	v_mfma_f32_16x16x32_bf16 v[98:101], v[94:97], v[18:21], 0
	v_mfma_f32_16x16x32_bf16 v[98:101], v[90:93], v[50:53], v[98:101]
	v_mfma_f32_16x16x32_bf16 v[102:105], v[94:97], v[22:25], 0
	v_fma_f32 v118, v158, |v78|, v118
	v_fma_f32 v119, v158, |v79|, v119
	v_fma_f32 v120, v158, |v80|, v120
	v_fma_f32 v121, v158, |v81|, v121
	v_fma_f32 v118, v160, |v82|, v118
	v_fma_f32 v119, v160, |v83|, v119
	v_fma_f32 v120, v160, |v84|, v120
	v_mfma_f32_16x16x32_bf16 v[102:105], v[90:93], v[54:57], v[102:105]
	v_fma_f32 v121, v160, |v85|, v121
	v_fma_f32 v118, v162, |v86|, v118
	v_fma_f32 v119, v162, |v87|, v119
	v_fma_f32 v120, v162, |v88|, v120
	v_fma_f32 v121, v162, |v89|, v121
	v_fma_f32 v118, v164, |v98|, v118
	v_fma_f32 v119, v164, |v99|, v119
	v_mfma_f32_16x16x32_bf16 v[224:227], v[94:97], v[26:29], 0
	v_fma_f32 v120, v164, |v100|, v120
	v_fma_f32 v121, v164, |v101|, v121
	v_mfma_f32_16x16x32_bf16 v[224:227], v[90:93], v[58:61], v[224:227]
	v_fma_f32 v118, v166, |v102|, v118
	v_fma_f32 v119, v166, |v103|, v119
	v_fma_f32 v120, v166, |v104|, v120
	v_fma_f32 v121, v166, |v105|, v121
	v_mfma_f32_16x16x32_bf16 v[228:231], v[94:97], v[30:33], 0
	v_mfma_f32_16x16x32_bf16 v[228:231], v[90:93], v[62:65], v[228:231]
	s_nop 4
	v_fma_f32 v118, v168, |v224|, v118
	v_fma_f32 v119, v168, |v225|, v119
	v_fma_f32 v120, v168, |v226|, v120
	v_fma_f32 v121, v168, |v227|, v121
	s_nop 1
	v_fma_f32 v118, v170, |v228|, v118
	v_fma_f32 v119, v170, |v229|, v119
	v_fma_f32 v120, v170, |v230|, v120
	v_fma_f32 v121, v170, |v231|, v121
	v_cvt_pk_f16_f32 v184, v118, v119
	v_cvt_pk_f16_f32 v185, v120, v121
	v_pk_ashrrev_i16 v186, 15, v184 op_sel_hi:[0,1]
	v_bitop3_b32 v182, v186, v184, s3 bitop3:0x36
	v_pk_ashrrev_i16 v186, 15, v185 op_sel_hi:[0,1]
	v_bitop3_b32 v183, v186, v185, s3 bitop3:0x36
	v_bfe_u32 v188, v182, 7, 9
	v_lshrrev_b32_e32 v189, 23, v182
	v_bfe_u32 v190, v183, 7, 9
	v_lshrrev_b32_e32 v191, 23, v183
	v_lshl_add_u32 v188, v188, 2, v143
	v_lshl_add_u32 v189, v189, 2, v143
	v_lshl_add_u32 v190, v190, 2, v143
	v_lshl_add_u32 v191, v191, 2, v143
	ds_add_u32 v188, v206
	ds_add_u32 v189, v206
	ds_add_u32 v190, v206
	ds_add_u32 v191, v206
	v_mov_b32_e32 v194, v157
	v_min_u32_e32 v194, 0x1fff, v194
	v_lshlrev_b32_e32 v140, 7, v194
	v_lshl_add_u64 v[192:193], v[172:173], 0, v[140:141]
	global_load_dwordx4 v[94:97], v[192:193], off
	global_load_dwordx4 v[90:93], v[192:193], off offset:1024
	v_add_u32_e32 v157, 0x100, v157
	ds_write2_b64 v195, v[176:177], v[178:179] offset1:4
	ds_write2_b64 v195, v[180:181], v[182:183] offset0:8 offset1:12
	s_waitcnt lgkmcnt(0)
	ds_read_b128 v[232:235], v196
	ds_read_b128 v[236:239], v196 offset:1152
	s_waitcnt lgkmcnt(1)
	global_store_dwordx4 v[174:175], v[232:235], off
	v_add_co_u32_e32 v198, vcc, s0, v174
	s_nop 1
	v_addc_co_u32_e32 v199, vcc, 0, v175, vcc
	s_waitcnt lgkmcnt(0)
	global_store_dwordx4 v[198:199], v[236:239], off
	v_lshl_add_u64 v[174:175], v[174:175], 0, s[14:15]
	s_cbranch_scc0 .LBB0_708
	s_waitcnt vmcnt(2)
	v_mov_b64_e32 v[118:119], v[134:135]
	v_mov_b64_e32 v[120:121], v[136:137]
	v_mov_b64_e32 v[114:115], v[130:131]
	v_mov_b64_e32 v[116:117], v[132:133]
	v_mov_b64_e32 v[102:103], v[126:127]
	v_mov_b64_e32 v[104:105], v[128:129]
	v_mov_b64_e32 v[98:99], v[122:123]
	v_mov_b64_e32 v[100:101], v[124:125]
	v_mov_b64_e32 v[86:87], v[110:111]
	v_mov_b64_e32 v[88:89], v[112:113]
	v_mov_b64_e32 v[82:83], v[106:107]
	v_mov_b64_e32 v[84:85], v[108:109]
	v_mov_b64_e32 v[78:79], v[94:95]
	v_mov_b64_e32 v[80:81], v[96:97]
	v_mov_b64_e32 v[74:75], v[90:91]
	v_mov_b64_e32 v[76:77], v[92:93]
	s_branch .LBB0_710

.LBB0_726:
	v_readlane_b32 s0, v255, 20
	v_readlane_b32 s1, v255, 21
	s_andn2_b64 vcc, exec, s[0:1]
	s_mov_b64 s[8:9], vcc
	s_cbranch_vccnz .LBB0_728
	v_cmp_ge_u32_sdwa vcc, v69, s22 src0_sel:WORD_0 src1_sel:DWORD
	s_mov_b32 s0, 0xfbff
	v_lshl_or_b32 v2, v69, 16, s0
	v_lshl_add_u32 v5, v91, 8, v79
	ds_write_b32 v5, v2
	v_addc_co_u32_e32 v91, vcc, 0, v91, vcc
	v_cmp_ge_u32_sdwa vcc, v69, s22 src0_sel:WORD_1 src1_sel:DWORD
	s_mov_b32 s1, 0xfbfe
	v_and_or_b32 v3, v69, v7, s1
	v_lshl_add_u32 v6, v91, 8, v79
	ds_write_b32 v6, v3
	v_addc_co_u32_e32 v91, vcc, 0, v91, vcc
	v_cmp_ge_u32_sdwa vcc, v68, s22 src0_sel:WORD_0 src1_sel:DWORD
	s_mov_b32 s0, 0xfb7f
	v_lshl_or_b32 v4, v68, 16, s0
	v_lshl_add_u32 v5, v91, 8, v79
	ds_write_b32 v5, v4
	v_addc_co_u32_e32 v91, vcc, 0, v91, vcc
	v_cmp_ge_u32_sdwa vcc, v68, s22 src0_sel:WORD_1 src1_sel:DWORD
	s_mov_b32 s1, 0xfb7e
	v_and_or_b32 v2, v68, v7, s1
	v_lshl_add_u32 v6, v91, 8, v79
	ds_write_b32 v6, v2
	v_addc_co_u32_e32 v91, vcc, 0, v91, vcc
	v_cmp_ge_u32_sdwa vcc, v67, s22 src0_sel:WORD_0 src1_sel:DWORD
	s_mov_b32 s0, 0xfaff
	v_lshl_or_b32 v3, v67, 16, s0
	v_lshl_add_u32 v5, v91, 8, v79
	ds_write_b32 v5, v3
	v_addc_co_u32_e32 v91, vcc, 0, v91, vcc
	v_cmp_ge_u32_sdwa vcc, v67, s22 src0_sel:WORD_1 src1_sel:DWORD
	s_mov_b32 s1, 0xfafe
	v_and_or_b32 v4, v67, v7, s1
	v_lshl_add_u32 v6, v91, 8, v79
	ds_write_b32 v6, v4
	v_addc_co_u32_e32 v91, vcc, 0, v91, vcc
	v_cmp_ge_u32_sdwa vcc, v66, s22 src0_sel:WORD_0 src1_sel:DWORD
	s_mov_b32 s0, 0xfa7f
	v_lshl_or_b32 v2, v66, 16, s0
	v_lshl_add_u32 v5, v91, 8, v79
	ds_write_b32 v5, v2
	v_addc_co_u32_e32 v91, vcc, 0, v91, vcc
	v_cmp_ge_u32_sdwa vcc, v66, s22 src0_sel:WORD_1 src1_sel:DWORD
	s_mov_b32 s1, 0xfa7e
	v_and_or_b32 v3, v66, v7, s1
	v_lshl_add_u32 v6, v91, 8, v79
	ds_write_b32 v6, v3
	v_addc_co_u32_e32 v91, vcc, 0, v91, vcc
	v_min_u32_e32 v91, 21, v91
	v_cmp_ge_u32_sdwa vcc, v65, s22 src0_sel:WORD_0 src1_sel:DWORD
	s_mov_b32 s0, 0xf9ff
	v_lshl_or_b32 v4, v65, 16, s0
	v_lshl_add_u32 v5, v91, 8, v79
	ds_write_b32 v5, v4
	v_addc_co_u32_e32 v91, vcc, 0, v91, vcc
	v_cmp_ge_u32_sdwa vcc, v65, s22 src0_sel:WORD_1 src1_sel:DWORD
	s_mov_b32 s1, 0xf9fe
	v_and_or_b32 v2, v65, v7, s1
	v_lshl_add_u32 v6, v91, 8, v79
	ds_write_b32 v6, v2
	v_addc_co_u32_e32 v91, vcc, 0, v91, vcc
	v_cmp_ge_u32_sdwa vcc, v64, s22 src0_sel:WORD_0 src1_sel:DWORD
	s_mov_b32 s0, 0xf97f
	v_lshl_or_b32 v3, v64, 16, s0
	v_lshl_add_u32 v5, v91, 8, v79
	ds_write_b32 v5, v3
	v_addc_co_u32_e32 v91, vcc, 0, v91, vcc
	v_cmp_ge_u32_sdwa vcc, v64, s22 src0_sel:WORD_1 src1_sel:DWORD
	s_mov_b32 s1, 0xf97e
	v_and_or_b32 v4, v64, v7, s1
	v_lshl_add_u32 v6, v91, 8, v79
	ds_write_b32 v6, v4
	v_addc_co_u32_e32 v91, vcc, 0, v91, vcc
	v_cmp_ge_u32_sdwa vcc, v63, s22 src0_sel:WORD_0 src1_sel:DWORD
	s_mov_b32 s0, 0xf8ff
	v_lshl_or_b32 v2, v63, 16, s0
	v_lshl_add_u32 v5, v91, 8, v79
	ds_write_b32 v5, v2
	v_addc_co_u32_e32 v91, vcc, 0, v91, vcc
	v_cmp_ge_u32_sdwa vcc, v63, s22 src0_sel:WORD_1 src1_sel:DWORD
	s_mov_b32 s1, 0xf8fe
	v_and_or_b32 v3, v63, v7, s1
	v_lshl_add_u32 v6, v91, 8, v79
	ds_write_b32 v6, v3
	v_addc_co_u32_e32 v91, vcc, 0, v91, vcc
	v_cmp_ge_u32_sdwa vcc, v62, s22 src0_sel:WORD_0 src1_sel:DWORD
	s_mov_b32 s0, 0xf87f
	v_lshl_or_b32 v4, v62, 16, s0
	v_lshl_add_u32 v5, v91, 8, v79
	ds_write_b32 v5, v4
	v_addc_co_u32_e32 v91, vcc, 0, v91, vcc
	v_cmp_ge_u32_sdwa vcc, v62, s22 src0_sel:WORD_1 src1_sel:DWORD
	s_mov_b32 s1, 0xf87e
	v_and_or_b32 v2, v62, v7, s1
	v_lshl_add_u32 v6, v91, 8, v79
	ds_write_b32 v6, v2
	v_addc_co_u32_e32 v91, vcc, 0, v91, vcc
	v_min_u32_e32 v91, 21, v91
.LBB0_728:
	v_readlane_b32 s0, v255, 22
	v_readlane_b32 s1, v255, 23
	s_andn2_b64 vcc, exec, s[0:1]
	s_mov_b64 s[10:11], vcc
	s_cbranch_vccnz .LBB0_730
	v_cmp_ge_u32_sdwa vcc, v61, s22 src0_sel:WORD_0 src1_sel:DWORD
	s_mov_b32 s0, 0xf7ff
	v_lshl_or_b32 v2, v61, 16, s0
	v_lshl_add_u32 v5, v91, 8, v79
	ds_write_b32 v5, v2
	v_addc_co_u32_e32 v91, vcc, 0, v91, vcc
	v_cmp_ge_u32_sdwa vcc, v61, s22 src0_sel:WORD_1 src1_sel:DWORD
	s_mov_b32 s1, 0xf7fe
	v_and_or_b32 v3, v61, v7, s1
	v_lshl_add_u32 v6, v91, 8, v79
	ds_write_b32 v6, v3
	v_addc_co_u32_e32 v91, vcc, 0, v91, vcc
	v_cmp_ge_u32_sdwa vcc, v60, s22 src0_sel:WORD_0 src1_sel:DWORD
	s_mov_b32 s0, 0xf77f
	v_lshl_or_b32 v4, v60, 16, s0
	v_lshl_add_u32 v5, v91, 8, v79
	ds_write_b32 v5, v4
	v_addc_co_u32_e32 v91, vcc, 0, v91, vcc
	v_cmp_ge_u32_sdwa vcc, v60, s22 src0_sel:WORD_1 src1_sel:DWORD
	s_mov_b32 s1, 0xf77e
	v_and_or_b32 v2, v60, v7, s1
	v_lshl_add_u32 v6, v91, 8, v79
	ds_write_b32 v6, v2
	v_addc_co_u32_e32 v91, vcc, 0, v91, vcc
	v_cmp_ge_u32_sdwa vcc, v59, s22 src0_sel:WORD_0 src1_sel:DWORD
	s_mov_b32 s0, 0xf6ff
	v_lshl_or_b32 v3, v59, 16, s0
	v_lshl_add_u32 v5, v91, 8, v79
	ds_write_b32 v5, v3
	v_addc_co_u32_e32 v91, vcc, 0, v91, vcc
	v_cmp_ge_u32_sdwa vcc, v59, s22 src0_sel:WORD_1 src1_sel:DWORD
	s_mov_b32 s1, 0xf6fe
	v_and_or_b32 v4, v59, v7, s1
	v_lshl_add_u32 v6, v91, 8, v79
	ds_write_b32 v6, v4
	v_addc_co_u32_e32 v91, vcc, 0, v91, vcc
	v_cmp_ge_u32_sdwa vcc, v58, s22 src0_sel:WORD_0 src1_sel:DWORD
	s_mov_b32 s0, 0xf67f
	v_lshl_or_b32 v2, v58, 16, s0
	v_lshl_add_u32 v5, v91, 8, v79
	ds_write_b32 v5, v2
	v_addc_co_u32_e32 v91, vcc, 0, v91, vcc
	v_cmp_ge_u32_sdwa vcc, v58, s22 src0_sel:WORD_1 src1_sel:DWORD
	s_mov_b32 s1, 0xf67e
	v_and_or_b32 v3, v58, v7, s1
	v_lshl_add_u32 v6, v91, 8, v79
	ds_write_b32 v6, v3
	v_addc_co_u32_e32 v91, vcc, 0, v91, vcc
	v_min_u32_e32 v91, 21, v91
	v_cmp_ge_u32_sdwa vcc, v57, s22 src0_sel:WORD_0 src1_sel:DWORD
	s_mov_b32 s0, 0xf5ff
	v_lshl_or_b32 v4, v57, 16, s0
	v_lshl_add_u32 v5, v91, 8, v79
	ds_write_b32 v5, v4
	v_addc_co_u32_e32 v91, vcc, 0, v91, vcc
	v_cmp_ge_u32_sdwa vcc, v57, s22 src0_sel:WORD_1 src1_sel:DWORD
	s_mov_b32 s1, 0xf5fe
	v_and_or_b32 v2, v57, v7, s1
	v_lshl_add_u32 v6, v91, 8, v79
	ds_write_b32 v6, v2
	v_addc_co_u32_e32 v91, vcc, 0, v91, vcc
	v_cmp_ge_u32_sdwa vcc, v56, s22 src0_sel:WORD_0 src1_sel:DWORD
	s_mov_b32 s0, 0xf57f
	v_lshl_or_b32 v3, v56, 16, s0
	v_lshl_add_u32 v5, v91, 8, v79
	ds_write_b32 v5, v3
	v_addc_co_u32_e32 v91, vcc, 0, v91, vcc
	v_cmp_ge_u32_sdwa vcc, v56, s22 src0_sel:WORD_1 src1_sel:DWORD
	s_mov_b32 s1, 0xf57e
	v_and_or_b32 v4, v56, v7, s1
	v_lshl_add_u32 v6, v91, 8, v79
	ds_write_b32 v6, v4
	v_addc_co_u32_e32 v91, vcc, 0, v91, vcc
	v_cmp_ge_u32_sdwa vcc, v55, s22 src0_sel:WORD_0 src1_sel:DWORD
	s_mov_b32 s0, 0xf4ff
	v_lshl_or_b32 v2, v55, 16, s0
	v_lshl_add_u32 v5, v91, 8, v79
	ds_write_b32 v5, v2
	v_addc_co_u32_e32 v91, vcc, 0, v91, vcc
	v_cmp_ge_u32_sdwa vcc, v55, s22 src0_sel:WORD_1 src1_sel:DWORD
	s_mov_b32 s1, 0xf4fe
	v_and_or_b32 v3, v55, v7, s1
	v_lshl_add_u32 v6, v91, 8, v79
	ds_write_b32 v6, v3
	v_addc_co_u32_e32 v91, vcc, 0, v91, vcc
	v_cmp_ge_u32_sdwa vcc, v54, s22 src0_sel:WORD_0 src1_sel:DWORD
	s_mov_b32 s0, 0xf47f
	v_lshl_or_b32 v4, v54, 16, s0
	v_lshl_add_u32 v5, v91, 8, v79
	ds_write_b32 v5, v4
	v_addc_co_u32_e32 v91, vcc, 0, v91, vcc
	v_cmp_ge_u32_sdwa vcc, v54, s22 src0_sel:WORD_1 src1_sel:DWORD
	s_mov_b32 s1, 0xf47e
	v_and_or_b32 v2, v54, v7, s1
	v_lshl_add_u32 v6, v91, 8, v79
	ds_write_b32 v6, v2
	v_addc_co_u32_e32 v91, vcc, 0, v91, vcc
	v_min_u32_e32 v91, 21, v91
.LBB0_730:
	v_readlane_b32 s0, v255, 24
	v_readlane_b32 s1, v255, 25
	s_andn2_b64 vcc, exec, s[0:1]
	s_mov_b64 s[12:13], vcc
	s_cbranch_vccnz .LBB0_732
	v_cmp_ge_u32_sdwa vcc, v53, s22 src0_sel:WORD_0 src1_sel:DWORD
	s_mov_b32 s0, 0xf3ff
	v_lshl_or_b32 v2, v53, 16, s0
	v_lshl_add_u32 v5, v91, 8, v79
	ds_write_b32 v5, v2
	v_addc_co_u32_e32 v91, vcc, 0, v91, vcc
	v_cmp_ge_u32_sdwa vcc, v53, s22 src0_sel:WORD_1 src1_sel:DWORD
	s_mov_b32 s1, 0xf3fe
	v_and_or_b32 v3, v53, v7, s1
	v_lshl_add_u32 v6, v91, 8, v79
	ds_write_b32 v6, v3
	v_addc_co_u32_e32 v91, vcc, 0, v91, vcc
	v_cmp_ge_u32_sdwa vcc, v52, s22 src0_sel:WORD_0 src1_sel:DWORD
	s_mov_b32 s0, 0xf37f
	v_lshl_or_b32 v4, v52, 16, s0
	v_lshl_add_u32 v5, v91, 8, v79
	ds_write_b32 v5, v4
	v_addc_co_u32_e32 v91, vcc, 0, v91, vcc
	v_cmp_ge_u32_sdwa vcc, v52, s22 src0_sel:WORD_1 src1_sel:DWORD
	s_mov_b32 s1, 0xf37e
	v_and_or_b32 v2, v52, v7, s1
	v_lshl_add_u32 v6, v91, 8, v79
	ds_write_b32 v6, v2
	v_addc_co_u32_e32 v91, vcc, 0, v91, vcc
	v_cmp_ge_u32_sdwa vcc, v51, s22 src0_sel:WORD_0 src1_sel:DWORD
	s_mov_b32 s0, 0xf2ff
	v_lshl_or_b32 v3, v51, 16, s0
	v_lshl_add_u32 v5, v91, 8, v79
	ds_write_b32 v5, v3
	v_addc_co_u32_e32 v91, vcc, 0, v91, vcc
	v_cmp_ge_u32_sdwa vcc, v51, s22 src0_sel:WORD_1 src1_sel:DWORD
	s_mov_b32 s1, 0xf2fe
	v_and_or_b32 v4, v51, v7, s1
	v_lshl_add_u32 v6, v91, 8, v79
	ds_write_b32 v6, v4
	v_addc_co_u32_e32 v91, vcc, 0, v91, vcc
	v_cmp_ge_u32_sdwa vcc, v50, s22 src0_sel:WORD_0 src1_sel:DWORD
	s_mov_b32 s0, 0xf27f
	v_lshl_or_b32 v2, v50, 16, s0
	v_lshl_add_u32 v5, v91, 8, v79
	ds_write_b32 v5, v2
	v_addc_co_u32_e32 v91, vcc, 0, v91, vcc
	v_cmp_ge_u32_sdwa vcc, v50, s22 src0_sel:WORD_1 src1_sel:DWORD
	s_mov_b32 s1, 0xf27e
	v_and_or_b32 v3, v50, v7, s1
	v_lshl_add_u32 v6, v91, 8, v79
	ds_write_b32 v6, v3
	v_addc_co_u32_e32 v91, vcc, 0, v91, vcc
	v_min_u32_e32 v91, 21, v91
	v_cmp_ge_u32_sdwa vcc, v49, s22 src0_sel:WORD_0 src1_sel:DWORD
	s_mov_b32 s0, 0xf1ff
	v_lshl_or_b32 v4, v49, 16, s0
	v_lshl_add_u32 v5, v91, 8, v79
	ds_write_b32 v5, v4
	v_addc_co_u32_e32 v91, vcc, 0, v91, vcc
	v_cmp_ge_u32_sdwa vcc, v49, s22 src0_sel:WORD_1 src1_sel:DWORD
	s_mov_b32 s1, 0xf1fe
	v_and_or_b32 v2, v49, v7, s1
	v_lshl_add_u32 v6, v91, 8, v79
	ds_write_b32 v6, v2
	v_addc_co_u32_e32 v91, vcc, 0, v91, vcc
	v_cmp_ge_u32_sdwa vcc, v48, s22 src0_sel:WORD_0 src1_sel:DWORD
	s_mov_b32 s0, 0xf17f
	v_lshl_or_b32 v3, v48, 16, s0
	v_lshl_add_u32 v5, v91, 8, v79
	ds_write_b32 v5, v3
	v_addc_co_u32_e32 v91, vcc, 0, v91, vcc
	v_cmp_ge_u32_sdwa vcc, v48, s22 src0_sel:WORD_1 src1_sel:DWORD
	s_mov_b32 s1, 0xf17e
	v_and_or_b32 v4, v48, v7, s1
	v_lshl_add_u32 v6, v91, 8, v79
	ds_write_b32 v6, v4
	v_addc_co_u32_e32 v91, vcc, 0, v91, vcc
	v_cmp_ge_u32_sdwa vcc, v47, s22 src0_sel:WORD_0 src1_sel:DWORD
	s_mov_b32 s0, 0xf0ff
	v_lshl_or_b32 v2, v47, 16, s0
	v_lshl_add_u32 v5, v91, 8, v79
	ds_write_b32 v5, v2
	v_addc_co_u32_e32 v91, vcc, 0, v91, vcc
	v_cmp_ge_u32_sdwa vcc, v47, s22 src0_sel:WORD_1 src1_sel:DWORD
	s_mov_b32 s1, 0xf0fe
	v_and_or_b32 v3, v47, v7, s1
	v_lshl_add_u32 v6, v91, 8, v79
	ds_write_b32 v6, v3
	v_addc_co_u32_e32 v91, vcc, 0, v91, vcc
	v_cmp_ge_u32_sdwa vcc, v46, s22 src0_sel:WORD_0 src1_sel:DWORD
	s_mov_b32 s0, 0xf07f
	v_lshl_or_b32 v4, v46, 16, s0
	v_lshl_add_u32 v5, v91, 8, v79
	ds_write_b32 v5, v4
	v_addc_co_u32_e32 v91, vcc, 0, v91, vcc
	v_cmp_ge_u32_sdwa vcc, v46, s22 src0_sel:WORD_1 src1_sel:DWORD
	s_mov_b32 s1, 0xf07e
	v_and_or_b32 v2, v46, v7, s1
	v_lshl_add_u32 v6, v91, 8, v79
	ds_write_b32 v6, v2
	v_addc_co_u32_e32 v91, vcc, 0, v91, vcc
	v_min_u32_e32 v91, 21, v91
.LBB0_732:
	v_readlane_b32 s0, v255, 26
	v_readlane_b32 s1, v255, 27
	s_andn2_b64 vcc, exec, s[0:1]
	s_mov_b64 s[14:15], vcc
	s_cbranch_vccnz .LBB0_734
	v_cmp_ge_u32_sdwa vcc, v45, s22 src0_sel:WORD_0 src1_sel:DWORD
	s_mov_b32 s0, 0xefff
	v_lshl_or_b32 v2, v45, 16, s0
	v_lshl_add_u32 v5, v91, 8, v79
	ds_write_b32 v5, v2
	v_addc_co_u32_e32 v91, vcc, 0, v91, vcc
	v_cmp_ge_u32_sdwa vcc, v45, s22 src0_sel:WORD_1 src1_sel:DWORD
	s_mov_b32 s1, 0xeffe
	v_and_or_b32 v3, v45, v7, s1
	v_lshl_add_u32 v6, v91, 8, v79
	ds_write_b32 v6, v3
	v_addc_co_u32_e32 v91, vcc, 0, v91, vcc
	v_cmp_ge_u32_sdwa vcc, v44, s22 src0_sel:WORD_0 src1_sel:DWORD
	s_mov_b32 s0, 0xef7f
	v_lshl_or_b32 v4, v44, 16, s0
	v_lshl_add_u32 v5, v91, 8, v79
	ds_write_b32 v5, v4
	v_addc_co_u32_e32 v91, vcc, 0, v91, vcc
	v_cmp_ge_u32_sdwa vcc, v44, s22 src0_sel:WORD_1 src1_sel:DWORD
	s_mov_b32 s1, 0xef7e
	v_and_or_b32 v2, v44, v7, s1
	v_lshl_add_u32 v6, v91, 8, v79
	ds_write_b32 v6, v2
	v_addc_co_u32_e32 v91, vcc, 0, v91, vcc
	v_cmp_ge_u32_sdwa vcc, v43, s22 src0_sel:WORD_0 src1_sel:DWORD
	s_mov_b32 s0, 0xeeff
	v_lshl_or_b32 v3, v43, 16, s0
	v_lshl_add_u32 v5, v91, 8, v79
	ds_write_b32 v5, v3
	v_addc_co_u32_e32 v91, vcc, 0, v91, vcc
	v_cmp_ge_u32_sdwa vcc, v43, s22 src0_sel:WORD_1 src1_sel:DWORD
	s_mov_b32 s1, 0xeefe
	v_and_or_b32 v4, v43, v7, s1
	v_lshl_add_u32 v6, v91, 8, v79
	ds_write_b32 v6, v4
	v_addc_co_u32_e32 v91, vcc, 0, v91, vcc
	v_cmp_ge_u32_sdwa vcc, v42, s22 src0_sel:WORD_0 src1_sel:DWORD
	s_mov_b32 s0, 0xee7f
	v_lshl_or_b32 v2, v42, 16, s0
	v_lshl_add_u32 v5, v91, 8, v79
	ds_write_b32 v5, v2
	v_addc_co_u32_e32 v91, vcc, 0, v91, vcc
	v_cmp_ge_u32_sdwa vcc, v42, s22 src0_sel:WORD_1 src1_sel:DWORD
	s_mov_b32 s1, 0xee7e
	v_and_or_b32 v3, v42, v7, s1
	v_lshl_add_u32 v6, v91, 8, v79
	ds_write_b32 v6, v3
	v_addc_co_u32_e32 v91, vcc, 0, v91, vcc
	v_min_u32_e32 v91, 21, v91
	v_cmp_ge_u32_sdwa vcc, v41, s22 src0_sel:WORD_0 src1_sel:DWORD
	s_mov_b32 s0, 0xedff
	v_lshl_or_b32 v4, v41, 16, s0
	v_lshl_add_u32 v5, v91, 8, v79
	ds_write_b32 v5, v4
	v_addc_co_u32_e32 v91, vcc, 0, v91, vcc
	v_cmp_ge_u32_sdwa vcc, v41, s22 src0_sel:WORD_1 src1_sel:DWORD
	s_mov_b32 s1, 0xedfe
	v_and_or_b32 v2, v41, v7, s1
	v_lshl_add_u32 v6, v91, 8, v79
	ds_write_b32 v6, v2
	v_addc_co_u32_e32 v91, vcc, 0, v91, vcc
	v_cmp_ge_u32_sdwa vcc, v40, s22 src0_sel:WORD_0 src1_sel:DWORD
	s_mov_b32 s0, 0xed7f
	v_lshl_or_b32 v3, v40, 16, s0
	v_lshl_add_u32 v5, v91, 8, v79
	ds_write_b32 v5, v3
	v_addc_co_u32_e32 v91, vcc, 0, v91, vcc
	v_cmp_ge_u32_sdwa vcc, v40, s22 src0_sel:WORD_1 src1_sel:DWORD
	s_mov_b32 s1, 0xed7e
	v_and_or_b32 v4, v40, v7, s1
	v_lshl_add_u32 v6, v91, 8, v79
	ds_write_b32 v6, v4
	v_addc_co_u32_e32 v91, vcc, 0, v91, vcc
	v_cmp_ge_u32_sdwa vcc, v39, s22 src0_sel:WORD_0 src1_sel:DWORD
	s_mov_b32 s0, 0xecff
	v_lshl_or_b32 v2, v39, 16, s0
	v_lshl_add_u32 v5, v91, 8, v79
	ds_write_b32 v5, v2
	v_addc_co_u32_e32 v91, vcc, 0, v91, vcc
	v_cmp_ge_u32_sdwa vcc, v39, s22 src0_sel:WORD_1 src1_sel:DWORD
	s_mov_b32 s1, 0xecfe
	v_and_or_b32 v3, v39, v7, s1
	v_lshl_add_u32 v6, v91, 8, v79
	ds_write_b32 v6, v3
	v_addc_co_u32_e32 v91, vcc, 0, v91, vcc
	v_cmp_ge_u32_sdwa vcc, v38, s22 src0_sel:WORD_0 src1_sel:DWORD
	s_mov_b32 s0, 0xec7f
	v_lshl_or_b32 v4, v38, 16, s0
	v_lshl_add_u32 v5, v91, 8, v79
	ds_write_b32 v5, v4
	v_addc_co_u32_e32 v91, vcc, 0, v91, vcc
	v_cmp_ge_u32_sdwa vcc, v38, s22 src0_sel:WORD_1 src1_sel:DWORD
	s_mov_b32 s1, 0xec7e
	v_and_or_b32 v2, v38, v7, s1
	v_lshl_add_u32 v6, v91, 8, v79
	ds_write_b32 v6, v2
	v_addc_co_u32_e32 v91, vcc, 0, v91, vcc
	v_min_u32_e32 v91, 21, v91
.LBB0_734:
	v_readlane_b32 s0, v255, 28
	v_readlane_b32 s1, v255, 29
	s_andn2_b64 vcc, exec, s[0:1]
	s_mov_b64 s[16:17], vcc
	s_cbranch_vccnz .LBB0_736
	v_cmp_ge_u32_sdwa vcc, v37, s22 src0_sel:WORD_0 src1_sel:DWORD
	s_mov_b32 s0, 0xebff
	v_lshl_or_b32 v2, v37, 16, s0
	v_lshl_add_u32 v5, v91, 8, v79
	ds_write_b32 v5, v2
	v_addc_co_u32_e32 v91, vcc, 0, v91, vcc
	v_cmp_ge_u32_sdwa vcc, v37, s22 src0_sel:WORD_1 src1_sel:DWORD
	s_mov_b32 s1, 0xebfe
	v_and_or_b32 v3, v37, v7, s1
	v_lshl_add_u32 v6, v91, 8, v79
	ds_write_b32 v6, v3
	v_addc_co_u32_e32 v91, vcc, 0, v91, vcc
	v_cmp_ge_u32_sdwa vcc, v36, s22 src0_sel:WORD_0 src1_sel:DWORD
	s_mov_b32 s0, 0xeb7f
	v_lshl_or_b32 v4, v36, 16, s0
	v_lshl_add_u32 v5, v91, 8, v79
	ds_write_b32 v5, v4
	v_addc_co_u32_e32 v91, vcc, 0, v91, vcc
	v_cmp_ge_u32_sdwa vcc, v36, s22 src0_sel:WORD_1 src1_sel:DWORD
	s_mov_b32 s1, 0xeb7e
	v_and_or_b32 v2, v36, v7, s1
	v_lshl_add_u32 v6, v91, 8, v79
	ds_write_b32 v6, v2
	v_addc_co_u32_e32 v91, vcc, 0, v91, vcc
	v_cmp_ge_u32_sdwa vcc, v35, s22 src0_sel:WORD_0 src1_sel:DWORD
	s_mov_b32 s0, 0xeaff
	v_lshl_or_b32 v3, v35, 16, s0
	v_lshl_add_u32 v5, v91, 8, v79
	ds_write_b32 v5, v3
	v_addc_co_u32_e32 v91, vcc, 0, v91, vcc
	v_cmp_ge_u32_sdwa vcc, v35, s22 src0_sel:WORD_1 src1_sel:DWORD
	s_mov_b32 s1, 0xeafe
	v_and_or_b32 v4, v35, v7, s1
	v_lshl_add_u32 v6, v91, 8, v79
	ds_write_b32 v6, v4
	v_addc_co_u32_e32 v91, vcc, 0, v91, vcc
	v_cmp_ge_u32_sdwa vcc, v34, s22 src0_sel:WORD_0 src1_sel:DWORD
	s_mov_b32 s0, 0xea7f
	v_lshl_or_b32 v2, v34, 16, s0
	v_lshl_add_u32 v5, v91, 8, v79
	ds_write_b32 v5, v2
	v_addc_co_u32_e32 v91, vcc, 0, v91, vcc
	v_cmp_ge_u32_sdwa vcc, v34, s22 src0_sel:WORD_1 src1_sel:DWORD
	s_mov_b32 s1, 0xea7e
	v_and_or_b32 v3, v34, v7, s1
	v_lshl_add_u32 v6, v91, 8, v79
	ds_write_b32 v6, v3
	v_addc_co_u32_e32 v91, vcc, 0, v91, vcc
	v_min_u32_e32 v91, 21, v91
	v_cmp_ge_u32_sdwa vcc, v33, s22 src0_sel:WORD_0 src1_sel:DWORD
	s_mov_b32 s0, 0xe9ff
	v_lshl_or_b32 v4, v33, 16, s0
	v_lshl_add_u32 v5, v91, 8, v79
	ds_write_b32 v5, v4
	v_addc_co_u32_e32 v91, vcc, 0, v91, vcc
	v_cmp_ge_u32_sdwa vcc, v33, s22 src0_sel:WORD_1 src1_sel:DWORD
	s_mov_b32 s1, 0xe9fe
	v_and_or_b32 v2, v33, v7, s1
	v_lshl_add_u32 v6, v91, 8, v79
	ds_write_b32 v6, v2
	v_addc_co_u32_e32 v91, vcc, 0, v91, vcc
	v_cmp_ge_u32_sdwa vcc, v32, s22 src0_sel:WORD_0 src1_sel:DWORD
	s_mov_b32 s0, 0xe97f
	v_lshl_or_b32 v3, v32, 16, s0
	v_lshl_add_u32 v5, v91, 8, v79
	ds_write_b32 v5, v3
	v_addc_co_u32_e32 v91, vcc, 0, v91, vcc
	v_cmp_ge_u32_sdwa vcc, v32, s22 src0_sel:WORD_1 src1_sel:DWORD
	s_mov_b32 s1, 0xe97e
	v_and_or_b32 v4, v32, v7, s1
	v_lshl_add_u32 v6, v91, 8, v79
	ds_write_b32 v6, v4
	v_addc_co_u32_e32 v91, vcc, 0, v91, vcc
	v_cmp_ge_u32_sdwa vcc, v31, s22 src0_sel:WORD_0 src1_sel:DWORD
	s_mov_b32 s0, 0xe8ff
	v_lshl_or_b32 v2, v31, 16, s0
	v_lshl_add_u32 v5, v91, 8, v79
	ds_write_b32 v5, v2
	v_addc_co_u32_e32 v91, vcc, 0, v91, vcc
	v_cmp_ge_u32_sdwa vcc, v31, s22 src0_sel:WORD_1 src1_sel:DWORD
	s_mov_b32 s1, 0xe8fe
	v_and_or_b32 v3, v31, v7, s1
	v_lshl_add_u32 v6, v91, 8, v79
	ds_write_b32 v6, v3
	v_addc_co_u32_e32 v91, vcc, 0, v91, vcc
	v_cmp_ge_u32_sdwa vcc, v30, s22 src0_sel:WORD_0 src1_sel:DWORD
	s_mov_b32 s0, 0xe87f
	v_lshl_or_b32 v4, v30, 16, s0
	v_lshl_add_u32 v5, v91, 8, v79
	ds_write_b32 v5, v4
	v_addc_co_u32_e32 v91, vcc, 0, v91, vcc
	v_cmp_ge_u32_sdwa vcc, v30, s22 src0_sel:WORD_1 src1_sel:DWORD
	s_mov_b32 s1, 0xe87e
	v_and_or_b32 v2, v30, v7, s1
	v_lshl_add_u32 v6, v91, 8, v79
	ds_write_b32 v6, v2
	v_addc_co_u32_e32 v91, vcc, 0, v91, vcc
	v_min_u32_e32 v91, 21, v91
.LBB0_736:
	v_readlane_b32 s0, v255, 30
	v_readlane_b32 s1, v255, 31
	s_andn2_b64 vcc, exec, s[0:1]
	s_mov_b64 s[18:19], vcc
	s_cbranch_vccnz .LBB0_738
	v_cmp_ge_u32_sdwa vcc, v29, s22 src0_sel:WORD_0 src1_sel:DWORD
	s_mov_b32 s0, 0xe7ff
	v_lshl_or_b32 v2, v29, 16, s0
	v_lshl_add_u32 v5, v91, 8, v79
	ds_write_b32 v5, v2
	v_addc_co_u32_e32 v91, vcc, 0, v91, vcc
	v_cmp_ge_u32_sdwa vcc, v29, s22 src0_sel:WORD_1 src1_sel:DWORD
	s_mov_b32 s1, 0xe7fe
	v_and_or_b32 v3, v29, v7, s1
	v_lshl_add_u32 v6, v91, 8, v79
	ds_write_b32 v6, v3
	v_addc_co_u32_e32 v91, vcc, 0, v91, vcc
	v_cmp_ge_u32_sdwa vcc, v28, s22 src0_sel:WORD_0 src1_sel:DWORD
	s_mov_b32 s0, 0xe77f
	v_lshl_or_b32 v4, v28, 16, s0
	v_lshl_add_u32 v5, v91, 8, v79
	ds_write_b32 v5, v4
	v_addc_co_u32_e32 v91, vcc, 0, v91, vcc
	v_cmp_ge_u32_sdwa vcc, v28, s22 src0_sel:WORD_1 src1_sel:DWORD
	s_mov_b32 s1, 0xe77e
	v_and_or_b32 v2, v28, v7, s1
	v_lshl_add_u32 v6, v91, 8, v79
	ds_write_b32 v6, v2
	v_addc_co_u32_e32 v91, vcc, 0, v91, vcc
	v_cmp_ge_u32_sdwa vcc, v27, s22 src0_sel:WORD_0 src1_sel:DWORD
	s_mov_b32 s0, 0xe6ff
	v_lshl_or_b32 v3, v27, 16, s0
	v_lshl_add_u32 v5, v91, 8, v79
	ds_write_b32 v5, v3
	v_addc_co_u32_e32 v91, vcc, 0, v91, vcc
	v_cmp_ge_u32_sdwa vcc, v27, s22 src0_sel:WORD_1 src1_sel:DWORD
	s_mov_b32 s1, 0xe6fe
	v_and_or_b32 v4, v27, v7, s1
	v_lshl_add_u32 v6, v91, 8, v79
	ds_write_b32 v6, v4
	v_addc_co_u32_e32 v91, vcc, 0, v91, vcc
	v_cmp_ge_u32_sdwa vcc, v26, s22 src0_sel:WORD_0 src1_sel:DWORD
	s_mov_b32 s0, 0xe67f
	v_lshl_or_b32 v2, v26, 16, s0
	v_lshl_add_u32 v5, v91, 8, v79
	ds_write_b32 v5, v2
	v_addc_co_u32_e32 v91, vcc, 0, v91, vcc
	v_cmp_ge_u32_sdwa vcc, v26, s22 src0_sel:WORD_1 src1_sel:DWORD
	s_mov_b32 s1, 0xe67e
	v_and_or_b32 v3, v26, v7, s1
	v_lshl_add_u32 v6, v91, 8, v79
	ds_write_b32 v6, v3
	v_addc_co_u32_e32 v91, vcc, 0, v91, vcc
	v_min_u32_e32 v91, 21, v91
	v_cmp_ge_u32_sdwa vcc, v25, s22 src0_sel:WORD_0 src1_sel:DWORD
	s_mov_b32 s0, 0xe5ff
	v_lshl_or_b32 v4, v25, 16, s0
	v_lshl_add_u32 v5, v91, 8, v79
	ds_write_b32 v5, v4
	v_addc_co_u32_e32 v91, vcc, 0, v91, vcc
	v_cmp_ge_u32_sdwa vcc, v25, s22 src0_sel:WORD_1 src1_sel:DWORD
	s_mov_b32 s1, 0xe5fe
	v_and_or_b32 v2, v25, v7, s1
	v_lshl_add_u32 v6, v91, 8, v79
	ds_write_b32 v6, v2
	v_addc_co_u32_e32 v91, vcc, 0, v91, vcc
	v_cmp_ge_u32_sdwa vcc, v24, s22 src0_sel:WORD_0 src1_sel:DWORD
	s_mov_b32 s0, 0xe57f
	v_lshl_or_b32 v3, v24, 16, s0
	v_lshl_add_u32 v5, v91, 8, v79
	ds_write_b32 v5, v3
	v_addc_co_u32_e32 v91, vcc, 0, v91, vcc
	v_cmp_ge_u32_sdwa vcc, v24, s22 src0_sel:WORD_1 src1_sel:DWORD
	s_mov_b32 s1, 0xe57e
	v_and_or_b32 v4, v24, v7, s1
	v_lshl_add_u32 v6, v91, 8, v79
	ds_write_b32 v6, v4
	v_addc_co_u32_e32 v91, vcc, 0, v91, vcc
	v_cmp_ge_u32_sdwa vcc, v23, s22 src0_sel:WORD_0 src1_sel:DWORD
	s_mov_b32 s0, 0xe4ff
	v_lshl_or_b32 v2, v23, 16, s0
	v_lshl_add_u32 v5, v91, 8, v79
	ds_write_b32 v5, v2
	v_addc_co_u32_e32 v91, vcc, 0, v91, vcc
	v_cmp_ge_u32_sdwa vcc, v23, s22 src0_sel:WORD_1 src1_sel:DWORD
	s_mov_b32 s1, 0xe4fe
	v_and_or_b32 v3, v23, v7, s1
	v_lshl_add_u32 v6, v91, 8, v79
	ds_write_b32 v6, v3
	v_addc_co_u32_e32 v91, vcc, 0, v91, vcc
	v_cmp_ge_u32_sdwa vcc, v22, s22 src0_sel:WORD_0 src1_sel:DWORD
	s_mov_b32 s0, 0xe47f
	v_lshl_or_b32 v4, v22, 16, s0
	v_lshl_add_u32 v5, v91, 8, v79
	ds_write_b32 v5, v4
	v_addc_co_u32_e32 v91, vcc, 0, v91, vcc
	v_cmp_ge_u32_sdwa vcc, v22, s22 src0_sel:WORD_1 src1_sel:DWORD
	s_mov_b32 s1, 0xe47e
	v_and_or_b32 v2, v22, v7, s1
	v_lshl_add_u32 v6, v91, 8, v79
	ds_write_b32 v6, v2
	v_addc_co_u32_e32 v91, vcc, 0, v91, vcc
	v_min_u32_e32 v91, 21, v91
.LBB0_738:
	v_readlane_b32 s0, v255, 32
	v_readlane_b32 s1, v255, 33
	s_andn2_b64 vcc, exec, s[0:1]
	s_mov_b64 s[20:21], vcc
	s_cbranch_vccnz .LBB0_740
	v_cmp_ge_u32_sdwa vcc, v21, s22 src0_sel:WORD_0 src1_sel:DWORD
	s_mov_b32 s0, 0xe3ff
	v_lshl_or_b32 v2, v21, 16, s0
	v_lshl_add_u32 v5, v91, 8, v79
	ds_write_b32 v5, v2
	v_addc_co_u32_e32 v91, vcc, 0, v91, vcc
	v_cmp_ge_u32_sdwa vcc, v21, s22 src0_sel:WORD_1 src1_sel:DWORD
	s_mov_b32 s1, 0xe3fe
	v_and_or_b32 v3, v21, v7, s1
	v_lshl_add_u32 v6, v91, 8, v79
	ds_write_b32 v6, v3
	v_addc_co_u32_e32 v91, vcc, 0, v91, vcc
	v_cmp_ge_u32_sdwa vcc, v20, s22 src0_sel:WORD_0 src1_sel:DWORD
	s_mov_b32 s0, 0xe37f
	v_lshl_or_b32 v4, v20, 16, s0
	v_lshl_add_u32 v5, v91, 8, v79
	ds_write_b32 v5, v4
	v_addc_co_u32_e32 v91, vcc, 0, v91, vcc
	v_cmp_ge_u32_sdwa vcc, v20, s22 src0_sel:WORD_1 src1_sel:DWORD
	s_mov_b32 s1, 0xe37e
	v_and_or_b32 v2, v20, v7, s1
	v_lshl_add_u32 v6, v91, 8, v79
	ds_write_b32 v6, v2
	v_addc_co_u32_e32 v91, vcc, 0, v91, vcc
	v_cmp_ge_u32_sdwa vcc, v19, s22 src0_sel:WORD_0 src1_sel:DWORD
	s_mov_b32 s0, 0xe2ff
	v_lshl_or_b32 v3, v19, 16, s0
	v_lshl_add_u32 v5, v91, 8, v79
	ds_write_b32 v5, v3
	v_addc_co_u32_e32 v91, vcc, 0, v91, vcc
	v_cmp_ge_u32_sdwa vcc, v19, s22 src0_sel:WORD_1 src1_sel:DWORD
	s_mov_b32 s1, 0xe2fe
	v_and_or_b32 v4, v19, v7, s1
	v_lshl_add_u32 v6, v91, 8, v79
	ds_write_b32 v6, v4
	v_addc_co_u32_e32 v91, vcc, 0, v91, vcc
	v_cmp_ge_u32_sdwa vcc, v18, s22 src0_sel:WORD_0 src1_sel:DWORD
	s_mov_b32 s0, 0xe27f
	v_lshl_or_b32 v2, v18, 16, s0
	v_lshl_add_u32 v5, v91, 8, v79
	ds_write_b32 v5, v2
	v_addc_co_u32_e32 v91, vcc, 0, v91, vcc
	v_cmp_ge_u32_sdwa vcc, v18, s22 src0_sel:WORD_1 src1_sel:DWORD
	s_mov_b32 s1, 0xe27e
	v_and_or_b32 v3, v18, v7, s1
	v_lshl_add_u32 v6, v91, 8, v79
	ds_write_b32 v6, v3
	v_addc_co_u32_e32 v91, vcc, 0, v91, vcc
	v_min_u32_e32 v91, 21, v91
	v_cmp_ge_u32_sdwa vcc, v17, s22 src0_sel:WORD_0 src1_sel:DWORD
	s_mov_b32 s0, 0xe1ff
	v_lshl_or_b32 v4, v17, 16, s0
	v_lshl_add_u32 v5, v91, 8, v79
	ds_write_b32 v5, v4
	v_addc_co_u32_e32 v91, vcc, 0, v91, vcc
	v_cmp_ge_u32_sdwa vcc, v17, s22 src0_sel:WORD_1 src1_sel:DWORD
	s_mov_b32 s1, 0xe1fe
	v_and_or_b32 v2, v17, v7, s1
	v_lshl_add_u32 v6, v91, 8, v79
	ds_write_b32 v6, v2
	v_addc_co_u32_e32 v91, vcc, 0, v91, vcc
	v_cmp_ge_u32_sdwa vcc, v16, s22 src0_sel:WORD_0 src1_sel:DWORD
	s_mov_b32 s0, 0xe17f
	v_lshl_or_b32 v3, v16, 16, s0
	v_lshl_add_u32 v5, v91, 8, v79
	ds_write_b32 v5, v3
	v_addc_co_u32_e32 v91, vcc, 0, v91, vcc
	v_cmp_ge_u32_sdwa vcc, v16, s22 src0_sel:WORD_1 src1_sel:DWORD
	s_mov_b32 s1, 0xe17e
	v_and_or_b32 v4, v16, v7, s1
	v_lshl_add_u32 v6, v91, 8, v79
	ds_write_b32 v6, v4
	v_addc_co_u32_e32 v91, vcc, 0, v91, vcc
	v_cmp_ge_u32_sdwa vcc, v15, s22 src0_sel:WORD_0 src1_sel:DWORD
	s_mov_b32 s0, 0xe0ff
	v_lshl_or_b32 v2, v15, 16, s0
	v_lshl_add_u32 v5, v91, 8, v79
	ds_write_b32 v5, v2
	v_addc_co_u32_e32 v91, vcc, 0, v91, vcc
	v_cmp_ge_u32_sdwa vcc, v15, s22 src0_sel:WORD_1 src1_sel:DWORD
	s_mov_b32 s1, 0xe0fe
	v_and_or_b32 v3, v15, v7, s1
	v_lshl_add_u32 v6, v91, 8, v79
	ds_write_b32 v6, v3
	v_addc_co_u32_e32 v91, vcc, 0, v91, vcc
	v_cmp_ge_u32_sdwa vcc, v14, s22 src0_sel:WORD_0 src1_sel:DWORD
	s_mov_b32 s0, 0xe07f
	v_lshl_or_b32 v4, v14, 16, s0
	v_lshl_add_u32 v5, v91, 8, v79
	ds_write_b32 v5, v4
	v_addc_co_u32_e32 v91, vcc, 0, v91, vcc
	v_cmp_ge_u32_sdwa vcc, v14, s22 src0_sel:WORD_1 src1_sel:DWORD
	s_mov_b32 s1, 0xe07e
	v_and_or_b32 v2, v14, v7, s1
	v_lshl_add_u32 v6, v91, 8, v79
	ds_write_b32 v6, v2
	v_addc_co_u32_e32 v91, vcc, 0, v91, vcc
	v_min_u32_e32 v91, 21, v91

.Lpad_skip:
	s_add_i32 s0, s97, s25
	s_ashr_i32 s1, s0, 31
	s_waitcnt lgkmcnt(0)
	s_lshl_b64 s[8:9], s[0:1], 10
	v_readlane_b32 s14, v254, 60
	v_lshl_add_u32 v2, v210, 1, s95
	v_ashrrev_i32_e32 v213, 3, v10
	v_and_b32_e32 v214, 7, v10
	s_add_u32 s8, s14, s8
	v_readlane_b32 s14, v254, 61
	v_and_b32_e32 v120, 7, v210
	ds_read_u16 v15, v2
	ds_read_u16 v32, v2 offset:32
	ds_read_u16 v38, v2 offset:64
	ds_read_u16 v39, v2 offset:96
	ds_read_u16 v40, v2 offset:128
	ds_read_u16 v41, v2 offset:160
	ds_read_u16 v54, v2 offset:192
	ds_read_u16 v55, v2 offset:224
	ds_read_u16 v56, v2 offset:256
	ds_read_u16 v14, v2 offset:288
	ds_read_u16 v13, v2 offset:320
	ds_read_u16 v12, v2 offset:352
	ds_read_u16 v9, v2 offset:384
	ds_read_u16 v8, v2 offset:416
	ds_read_u16 v7, v2 offset:448
	ds_read_u16 v6, v2 offset:480
	s_addc_u32 s9, s14, s9
	v_lshl_add_u32 v212, v213, 1, s95
	v_lshlrev_b32_e32 v140, 7, v120
	v_lshlrev_b32_e32 v24, 4, v211
	v_lshl_add_u64 v[2:3], s[8:9], 0, v[140:141]
	v_ashrrev_i32_e32 v25, 31, v24
	v_lshl_add_u64 v[2:3], v[24:25], 1, v[2:3]
	global_load_dwordx4 v[16:19], v[2:3], off
	global_load_dwordx4 v[20:23], v[2:3], off offset:16
	ds_read_u16 v5, v212
	ds_read_u16 v4, v212 offset:16
	ds_read_u16 v11, v212 offset:32
	ds_read_u16 v10, v212 offset:48
	s_waitcnt lgkmcnt(0)
	v_lshl_add_u64 v[2:3], s[46:47], 0, v[24:25]
	s_waitcnt lgkmcnt(0)
	v_lshl_add_u32 v244, v15, 7, v24
	global_load_dwordx4 v[156:159], v244, s[46:47]
	global_load_dwordx4 v[160:163], v244, s[46:47] offset:64
	v_lshl_add_u32 v244, v32, 7, v24
	global_load_dwordx4 v[164:167], v244, s[46:47]
	global_load_dwordx4 v[168:171], v244, s[46:47] offset:64
	v_lshl_add_u32 v244, v38, 7, v24
	global_load_dwordx4 v[172:175], v244, s[46:47]
	global_load_dwordx4 v[176:179], v244, s[46:47] offset:64
	v_lshl_add_u32 v244, v39, 7, v24
	global_load_dwordx4 v[180:183], v244, s[46:47]
	global_load_dwordx4 v[184:187], v244, s[46:47] offset:64
	v_lshl_add_u32 v244, v40, 7, v24
	global_load_dwordx4 v[188:191], v244, s[46:47]
	global_load_dwordx4 v[192:195], v244, s[46:47] offset:64
	v_lshl_add_u32 v244, v41, 7, v24
	global_load_dwordx4 v[196:199], v244, s[46:47]
	global_load_dwordx4 v[224:227], v244, s[46:47] offset:64
	v_lshl_add_u32 v244, v54, 7, v24
	global_load_dwordx4 v[228:231], v244, s[46:47]
	global_load_dwordx4 v[232:235], v244, s[46:47] offset:64
	v_lshl_add_u32 v244, v55, 7, v24
	global_load_dwordx4 v[236:239], v244, s[46:47]
	global_load_dwordx4 v[240:243], v244, s[46:47] offset:64
	v_mov_b32_e32 v15, v141
	v_mov_b32_e32 v42, v141
	v_mov_b32_e32 v43, v141
	v_mov_b32_e32 v44, v141
	v_lshlrev_b32_e32 v116, 4, v214
	v_ashrrev_i32_e32 v117, 31, v116
	v_lshl_add_u64 v[114:115], s[48:49], 0, v[116:117]
	v_lshl_add_u32 v121, v211, 3, s95
	v_lshlrev_b32_e32 v117, 2, v211
	ds_read2_b64 v[110:113], v121 offset1:4
	ds_read2_b64 v[106:109], v121 offset0:8 offset1:12
	ds_read2_b64 v[102:105], v121 offset0:16 offset1:20
	ds_read2_b64 v[98:101], v121 offset0:24 offset1:28
	ds_read2_b64 v[94:97], v121 offset0:32 offset1:36
	ds_read2_b64 v[90:93], v121 offset0:40 offset1:44
	ds_read2_b64 v[86:89], v121 offset0:48 offset1:52
	s_waitcnt vmcnt(16)
	v_lshlrev_b32_e32 v45, 16, v16
	v_and_b32_e32 v16, 0xffff0000, v16
	v_lshlrev_b32_e32 v47, 16, v18
	v_and_b32_e32 v18, 0xffff0000, v18
	v_lshlrev_b32_e32 v49, 16, v20
	v_and_b32_e32 v20, 0xffff0000, v20
	v_lshlrev_b32_e32 v51, 16, v22
	v_and_b32_e32 v22, 0xffff0000, v22
	v_mul_f32_e32 v45, 0x41000000, v45
	v_mul_f32_e32 v16, 0x41000000, v16
	v_mul_f32_e32 v47, 0x41000000, v47
	v_mul_f32_e32 v18, 0x41000000, v18
	v_mul_f32_e32 v49, 0x41000000, v49
	v_mul_f32_e32 v20, 0x41000000, v20
	v_mul_f32_e32 v51, 0x41000000, v51
	v_mul_f32_e32 v22, 0x41000000, v22
	v_cvt_pk_fp8_f32 v15, v45, v16
	v_cvt_pk_fp8_f32 v42, v47, v18
	v_cvt_pk_fp8_f32 v43, v49, v20
	v_cvt_pk_fp8_f32 v44, v51, v22
	v_lshlrev_b32_e32 v46, 16, v17
	v_and_b32_e32 v17, 0xffff0000, v17
	v_lshlrev_b32_e32 v48, 16, v19
	v_and_b32_e32 v19, 0xffff0000, v19
	v_lshlrev_b32_e32 v50, 16, v21
	v_and_b32_e32 v21, 0xffff0000, v21
	v_lshlrev_b32_e32 v52, 16, v23
	v_and_b32_e32 v23, 0xffff0000, v23
	v_mul_f32_e32 v46, 0x41000000, v46
	v_mul_f32_e32 v17, 0x41000000, v17
	v_mul_f32_e32 v48, 0x41000000, v48
	v_mul_f32_e32 v19, 0x41000000, v19
	v_mul_f32_e32 v50, 0x41000000, v50
	v_mul_f32_e32 v21, 0x41000000, v21
	v_mul_f32_e32 v52, 0x41000000, v52
	v_mul_f32_e32 v23, 0x41000000, v23
	v_cvt_pk_fp8_f32 v15, v46, v17 op_sel:[0,0,1]
	v_cvt_pk_fp8_f32 v42, v48, v19 op_sel:[0,0,1]
	v_cvt_pk_fp8_f32 v43, v50, v21 op_sel:[0,0,1]
	v_cvt_pk_fp8_f32 v44, v52, v23 op_sel:[0,0,1]
	v_and_b32_e32 v20, -4, v210
	v_cmp_gt_u32_e32 vcc, 4, v210
	s_nop 1
	v_cndmask_b32_e32 v75, 0, v42, vcc
	v_cndmask_b32_e32 v74, 0, v15, vcc
	v_cndmask_b32_e32 v83, 0, v44, vcc
	v_cndmask_b32_e32 v82, 0, v43, vcc
	v_cmp_eq_u32_e32 vcc, 4, v20
	s_nop 1
	v_cndmask_b32_e32 v77, 0, v42, vcc
	v_cndmask_b32_e32 v76, 0, v15, vcc
	v_cndmask_b32_e32 v119, 0, v44, vcc
	v_cndmask_b32_e32 v118, 0, v43, vcc
	s_nop 1
	s_waitcnt vmcnt(14)
	v_mfma_f32_16x16x32_fp8_fp8 v[30:33], v[156:157], v[74:75], 0
	v_mfma_f32_16x16x32_fp8_fp8 v[30:33], v[158:159], v[82:83], v[30:33]
	v_mfma_f32_16x16x32_fp8_fp8 v[30:33], v[160:161], v[76:77], v[30:33]
	v_mfma_f32_16x16x32_fp8_fp8 v[30:33], v[162:163], v[118:119], v[30:33]
	v_lshl_add_u32 v244, v56, 7, v24
	global_load_dwordx4 v[156:159], v244, s[46:47]
	global_load_dwordx4 v[160:163], v244, s[46:47] offset:64
	s_waitcnt vmcnt(14)
	v_mfma_f32_16x16x32_fp8_fp8 v[42:45], v[164:165], v[74:75], 0
	v_mfma_f32_16x16x32_fp8_fp8 v[42:45], v[166:167], v[82:83], v[42:45]
	v_mfma_f32_16x16x32_fp8_fp8 v[42:45], v[168:169], v[76:77], v[42:45]
	v_mfma_f32_16x16x32_fp8_fp8 v[42:45], v[170:171], v[118:119], v[42:45]
	v_lshl_add_u32 v244, v14, 7, v24
	global_load_dwordx4 v[164:167], v244, s[46:47]
	global_load_dwordx4 v[168:171], v244, s[46:47] offset:64
	s_waitcnt vmcnt(14)
	v_mfma_f32_16x16x32_fp8_fp8 v[46:49], v[172:173], v[74:75], 0
	v_mfma_f32_16x16x32_fp8_fp8 v[46:49], v[174:175], v[82:83], v[46:49]
	v_mfma_f32_16x16x32_fp8_fp8 v[46:49], v[176:177], v[76:77], v[46:49]
	v_mfma_f32_16x16x32_fp8_fp8 v[46:49], v[178:179], v[118:119], v[46:49]
	v_lshl_add_u32 v244, v13, 7, v24
	global_load_dwordx4 v[172:175], v244, s[46:47]
	global_load_dwordx4 v[176:179], v244, s[46:47] offset:64
	s_waitcnt vmcnt(14)
	v_mfma_f32_16x16x32_fp8_fp8 v[50:53], v[180:181], v[74:75], 0
	v_mfma_f32_16x16x32_fp8_fp8 v[50:53], v[182:183], v[82:83], v[50:53]
	v_mfma_f32_16x16x32_fp8_fp8 v[50:53], v[184:185], v[76:77], v[50:53]
	v_mfma_f32_16x16x32_fp8_fp8 v[50:53], v[186:187], v[118:119], v[50:53]
	v_lshl_add_u32 v244, v12, 7, v24
	global_load_dwordx4 v[180:183], v244, s[46:47]
	global_load_dwordx4 v[184:187], v244, s[46:47] offset:64
	s_waitcnt vmcnt(14)
	v_mfma_f32_16x16x32_fp8_fp8 v[58:61], v[188:189], v[74:75], 0
	v_mfma_f32_16x16x32_fp8_fp8 v[58:61], v[190:191], v[82:83], v[58:61]
	v_mfma_f32_16x16x32_fp8_fp8 v[58:61], v[192:193], v[76:77], v[58:61]
	v_mfma_f32_16x16x32_fp8_fp8 v[58:61], v[194:195], v[118:119], v[58:61]
	v_lshl_add_u32 v244, v9, 7, v24
	global_load_dwordx4 v[188:191], v244, s[46:47]
	global_load_dwordx4 v[192:195], v244, s[46:47] offset:64
	s_waitcnt vmcnt(14)
	v_mfma_f32_16x16x32_fp8_fp8 v[62:65], v[196:197], v[74:75], 0
	v_mfma_f32_16x16x32_fp8_fp8 v[62:65], v[198:199], v[82:83], v[62:65]
	v_mfma_f32_16x16x32_fp8_fp8 v[62:65], v[224:225], v[76:77], v[62:65]
	v_mfma_f32_16x16x32_fp8_fp8 v[62:65], v[226:227], v[118:119], v[62:65]
	v_lshl_add_u32 v244, v8, 7, v24
	global_load_dwordx4 v[196:199], v244, s[46:47]
	global_load_dwordx4 v[224:227], v244, s[46:47] offset:64
	s_waitcnt vmcnt(14)
	v_mfma_f32_16x16x32_fp8_fp8 v[70:73], v[228:229], v[74:75], 0
	v_mfma_f32_16x16x32_fp8_fp8 v[70:73], v[230:231], v[82:83], v[70:73]
	v_mfma_f32_16x16x32_fp8_fp8 v[70:73], v[232:233], v[76:77], v[70:73]
	v_mfma_f32_16x16x32_fp8_fp8 v[70:73], v[234:235], v[118:119], v[70:73]
	v_lshl_add_u32 v244, v7, 7, v24
	global_load_dwordx4 v[228:231], v244, s[46:47]
	global_load_dwordx4 v[232:235], v244, s[46:47] offset:64
	s_waitcnt vmcnt(14)
	v_mfma_f32_16x16x32_fp8_fp8 v[78:81], v[236:237], v[74:75], 0
	v_mfma_f32_16x16x32_fp8_fp8 v[78:81], v[238:239], v[82:83], v[78:81]
	v_mfma_f32_16x16x32_fp8_fp8 v[78:81], v[240:241], v[76:77], v[78:81]
	v_mfma_f32_16x16x32_fp8_fp8 v[78:81], v[242:243], v[118:119], v[78:81]
	v_lshl_add_u32 v244, v6, 7, v24
	global_load_dwordx4 v[236:239], v244, s[46:47]
	global_load_dwordx4 v[240:243], v244, s[46:47] offset:64
	v_lshl_add_u32 v246, v5, 7, v116
	v_lshl_add_u32 v248, v4, 7, v116
	v_lshl_add_u32 v250, v11, 7, v116
	v_lshl_add_u32 v252, v10, 7, v116
	global_load_dwordx4 v[2:5], v246, s[48:49]
	global_load_dwordx4 v[6:9], v248, s[48:49]
	global_load_dwordx4 v[10:13], v250, s[48:49]
	global_load_dwordx4 v[14:17], v252, s[48:49]
	s_waitcnt vmcnt(18)
	v_mfma_f32_16x16x32_fp8_fp8 v[18:21], v[156:157], v[74:75], 0
	v_mfma_f32_16x16x32_fp8_fp8 v[18:21], v[158:159], v[82:83], v[18:21]
	v_mfma_f32_16x16x32_fp8_fp8 v[18:21], v[160:161], v[76:77], v[18:21]
	v_mfma_f32_16x16x32_fp8_fp8 v[18:21], v[162:163], v[118:119], v[18:21]
	s_waitcnt vmcnt(16)
	v_mfma_f32_16x16x32_fp8_fp8 v[22:25], v[164:165], v[74:75], 0
	v_mfma_f32_16x16x32_fp8_fp8 v[22:25], v[166:167], v[82:83], v[22:25]
	v_mfma_f32_16x16x32_fp8_fp8 v[22:25], v[168:169], v[76:77], v[22:25]
	v_mfma_f32_16x16x32_fp8_fp8 v[22:25], v[170:171], v[118:119], v[22:25]
	s_waitcnt vmcnt(14)
	v_mfma_f32_16x16x32_fp8_fp8 v[26:29], v[172:173], v[74:75], 0
	v_mfma_f32_16x16x32_fp8_fp8 v[26:29], v[174:175], v[82:83], v[26:29]
	v_mfma_f32_16x16x32_fp8_fp8 v[26:29], v[176:177], v[76:77], v[26:29]
	v_mfma_f32_16x16x32_fp8_fp8 v[26:29], v[178:179], v[118:119], v[26:29]
	s_waitcnt vmcnt(12)
	v_mfma_f32_16x16x32_fp8_fp8 v[34:37], v[180:181], v[74:75], 0
	v_mfma_f32_16x16x32_fp8_fp8 v[34:37], v[182:183], v[82:83], v[34:37]
	v_mfma_f32_16x16x32_fp8_fp8 v[34:37], v[184:185], v[76:77], v[34:37]
	v_mfma_f32_16x16x32_fp8_fp8 v[34:37], v[186:187], v[118:119], v[34:37]
	s_waitcnt vmcnt(10)
	v_mfma_f32_16x16x32_fp8_fp8 v[38:41], v[188:189], v[74:75], 0
	v_mfma_f32_16x16x32_fp8_fp8 v[38:41], v[190:191], v[82:83], v[38:41]
	v_mfma_f32_16x16x32_fp8_fp8 v[38:41], v[192:193], v[76:77], v[38:41]
	v_mfma_f32_16x16x32_fp8_fp8 v[38:41], v[194:195], v[118:119], v[38:41]
	s_waitcnt vmcnt(8)
	v_mfma_f32_16x16x32_fp8_fp8 v[54:57], v[196:197], v[74:75], 0
	v_mfma_f32_16x16x32_fp8_fp8 v[54:57], v[198:199], v[82:83], v[54:57]
	v_mfma_f32_16x16x32_fp8_fp8 v[54:57], v[224:225], v[76:77], v[54:57]
	v_mfma_f32_16x16x32_fp8_fp8 v[54:57], v[226:227], v[118:119], v[54:57]
	s_waitcnt vmcnt(6)
	v_mfma_f32_16x16x32_fp8_fp8 v[66:69], v[228:229], v[74:75], 0
	v_mfma_f32_16x16x32_fp8_fp8 v[66:69], v[230:231], v[82:83], v[66:69]
	v_mfma_f32_16x16x32_fp8_fp8 v[66:69], v[232:233], v[76:77], v[66:69]
	v_mfma_f32_16x16x32_fp8_fp8 v[66:69], v[234:235], v[118:119], v[66:69]
	s_waitcnt vmcnt(4)
	v_mfma_f32_16x16x32_fp8_fp8 v[248:251], v[236:237], v[74:75], 0
	v_mfma_f32_16x16x32_fp8_fp8 v[248:251], v[238:239], v[82:83], v[248:251]
	v_mfma_f32_16x16x32_fp8_fp8 v[74:77], v[240:241], v[76:77], v[248:251]
	v_mfma_f32_16x16x32_fp8_fp8 v[74:77], v[242:243], v[118:119], v[74:77]
	s_nop 7
	ds_read2_b64 v[82:85], v121 offset0:56 offset1:60
	v_lshl_add_u32 v140, v120, 2, s22
	s_waitcnt lgkmcnt(0)
	s_cmpk_lt_i32 s97, 0xff
	s_mov_b64 s[8:9], -1
	s_cbranch_scc0 .LBB0_1332
	v_cmp_ge_i32_e32 vcc, s10, v117
	v_mov_b32_e32 v119, 0xff800000
	v_mov_b32_e32 v118, 0xff800000
	s_and_saveexec_b64 s[8:9], vcc
	s_cbranch_execz .LBB0_1205
	s_waitcnt lgkmcnt(7)
	v_sub_u32_sdwa v118, s97, v110 dst_sel:DWORD dst_unused:UNUSED_PAD src0_sel:DWORD src1_sel:WORD_0
	v_min_i32_e32 v118, 0x71, v118
	v_lshl_add_u32 v118, v118, 5, v140
	ds_read_b32 v118, v118
	s_waitcnt lgkmcnt(0)
	v_fmac_f32_e32 v118, 0x3e000000, v30
